# first K-tile of each GEMM unit (ui>=1) peeled: vmcnt waits relaxed so they do not wait on the previous epilogue's stores (7 K-loops)
# speedup vs baseline: 1.0014x; 1.0014x over previous
.LBB0_270:
	s_or_b64 exec, exec, s[48:49]
	s_ashr_i32 s27, s26, 31
	s_lshl_b64 s[48:49], s[26:27], 19
	s_add_u32 s48, s80, s48
	s_addc_u32 s49, s81, s49
	s_and_b64 s[50:51], s[46:47], exec
	s_cselect_b32 s27, s49, s55
	s_cselect_b32 s53, s48, s54
	s_ashr_i32 s31, s30, 31
	s_lshl_b64 s[50:51], s[30:31], 19
	s_add_u32 s50, s1, s50
	s_addc_u32 s51, s0, s51
	s_and_b64 s[58:59], s[46:47], exec
	s_cselect_b32 s31, s51, s57
	s_cselect_b32 s67, s50, s56
	s_add_u32 s54, s54, 0x40080
	s_addc_u32 s55, s55, 0
	s_add_u32 s68, s56, 0x100
	v_mov_b32_e32 v0, 0
	s_addc_u32 s69, s57, 0
	s_mov_b32 s70, -2
	v_mov_b32_e32 v1, v0
	v_mov_b32_e32 v2, v0
	v_mov_b32_e32 v3, v0
	v_mov_b32_e32 v4, v0
	v_mov_b32_e32 v5, v0
	v_mov_b32_e32 v6, v0
	v_mov_b32_e32 v7, v0
	v_mov_b32_e32 v16, v0
	v_mov_b32_e32 v17, v0
	v_mov_b32_e32 v18, v0
	v_mov_b32_e32 v19, v0
	v_mov_b32_e32 v20, v0
	v_mov_b32_e32 v21, v0
	v_mov_b32_e32 v22, v0
	v_mov_b32_e32 v23, v0
	v_mov_b32_e32 v32, v0
	v_mov_b32_e32 v33, v0
	v_mov_b32_e32 v34, v0
	v_mov_b32_e32 v35, v0
	v_mov_b32_e32 v36, v0
	v_mov_b32_e32 v37, v0
	v_mov_b32_e32 v38, v0
	v_mov_b32_e32 v39, v0
	v_mov_b32_e32 v48, v0
	v_mov_b32_e32 v49, v0
	v_mov_b32_e32 v50, v0
	v_mov_b32_e32 v51, v0
	v_mov_b32_e32 v52, v0
	v_mov_b32_e32 v53, v0
	v_mov_b32_e32 v54, v0
	v_mov_b32_e32 v55, v0
	v_mov_b32_e32 v8, v0
	v_mov_b32_e32 v9, v0
	v_mov_b32_e32 v10, v0
	v_mov_b32_e32 v11, v0
	v_mov_b32_e32 v12, v0
	v_mov_b32_e32 v13, v0
	v_mov_b32_e32 v14, v0
	v_mov_b32_e32 v15, v0
	v_mov_b32_e32 v24, v0
	v_mov_b32_e32 v25, v0
	v_mov_b32_e32 v26, v0
	v_mov_b32_e32 v27, v0
	v_mov_b32_e32 v28, v0
	v_mov_b32_e32 v29, v0
	v_mov_b32_e32 v30, v0
	v_mov_b32_e32 v31, v0
	v_mov_b32_e32 v40, v0
	v_mov_b32_e32 v41, v0
	v_mov_b32_e32 v42, v0
	v_mov_b32_e32 v43, v0
	v_mov_b32_e32 v44, v0
	v_mov_b32_e32 v45, v0
	v_mov_b32_e32 v46, v0
	v_mov_b32_e32 v47, v0
	v_mov_b32_e32 v56, v0
	v_mov_b32_e32 v57, v0
	v_mov_b32_e32 v58, v0
	v_mov_b32_e32 v59, v0
	v_mov_b32_e32 v60, v0
	v_mov_b32_e32 v61, v0
	v_mov_b32_e32 v62, v0
	v_mov_b32_e32 v63, v0
	v_mov_b32_e32 v64, v0
	v_mov_b32_e32 v65, v0
	v_mov_b32_e32 v66, v0
	v_mov_b32_e32 v67, v0
	v_mov_b32_e32 v68, v0
	v_mov_b32_e32 v69, v0
	v_mov_b32_e32 v70, v0
	v_mov_b32_e32 v71, v0
	v_mov_b32_e32 v80, v0
	v_mov_b32_e32 v81, v0
	v_mov_b32_e32 v82, v0
	v_mov_b32_e32 v83, v0
	v_mov_b32_e32 v84, v0
	v_mov_b32_e32 v85, v0
	v_mov_b32_e32 v86, v0
	v_mov_b32_e32 v87, v0
	v_mov_b32_e32 v96, v0
	v_mov_b32_e32 v97, v0
	v_mov_b32_e32 v98, v0
	v_mov_b32_e32 v99, v0
	v_mov_b32_e32 v100, v0
	v_mov_b32_e32 v101, v0
	v_mov_b32_e32 v102, v0
	v_mov_b32_e32 v103, v0
	v_mov_b32_e32 v112, v0
	v_mov_b32_e32 v113, v0
	v_mov_b32_e32 v114, v0
	v_mov_b32_e32 v115, v0
	v_mov_b32_e32 v116, v0
	v_mov_b32_e32 v117, v0
	v_mov_b32_e32 v118, v0
	v_mov_b32_e32 v119, v0
	v_mov_b32_e32 v72, v0
	v_mov_b32_e32 v73, v0
	v_mov_b32_e32 v74, v0
	v_mov_b32_e32 v75, v0
	v_mov_b32_e32 v76, v0
	v_mov_b32_e32 v77, v0
	v_mov_b32_e32 v78, v0
	v_mov_b32_e32 v79, v0
	v_mov_b32_e32 v88, v0
	v_mov_b32_e32 v89, v0
	v_mov_b32_e32 v90, v0
	v_mov_b32_e32 v91, v0
	v_mov_b32_e32 v92, v0
	v_mov_b32_e32 v93, v0
	v_mov_b32_e32 v94, v0
	v_mov_b32_e32 v95, v0
	v_mov_b32_e32 v104, v0
	v_mov_b32_e32 v105, v0
	v_mov_b32_e32 v106, v0
	v_mov_b32_e32 v107, v0
	v_mov_b32_e32 v108, v0
	v_mov_b32_e32 v109, v0
	v_mov_b32_e32 v110, v0
	v_mov_b32_e32 v111, v0
	v_mov_b32_e32 v120, v0
	v_mov_b32_e32 v121, v0
	v_mov_b32_e32 v122, v0
	v_mov_b32_e32 v123, v0
	v_mov_b32_e32 v124, v0
	v_mov_b32_e32 v125, v0
	v_mov_b32_e32 v126, v0
	v_mov_b32_e32 v127, v0
	s_cmp_eq_u32 s9, 0
	s_cbranch_scc1 .LBB0_271
	s_add_u32 s56, s54, 0xfffc0080
	s_addc_u32 s57, s55, -1
	s_add_i32 s71, 0, 0x10000
	s_cmp_eq_u32 s70, 12
	s_cselect_b32 s59, s27, s57
	s_cselect_b32 s58, s53, s56
	v_add_u32_e32 v144, s71, v158
	s_cselect_b32 s57, s31, s69
	s_cselect_b32 s56, s67, s68
	s_add_i32 s76, 0, 0x14000
	ds_read_b128 v[164:167], v144
	ds_read_b128 v[168:171], v144 offset:1024
	ds_read_b128 v[172:175], v144 offset:2048
	ds_read_b128 v[176:179], v144 offset:3072
	v_add_u32_e32 v144, s76, v158
	ds_read_b128 v[180:183], v144
	ds_read_b128 v[184:187], v144 offset:1024
	ds_read_b128 v[188:191], v144 offset:2048
	ds_read_b128 v[192:195], v144 offset:3072
	v_lshl_add_u64 v[144:145], s[54:55], 0, v[140:141]
	s_add_i32 m0, s60, 0xc000
	ds_read_b128 v[200:203], v162
	ds_read_b128 v[216:219], v162 offset:1024
	ds_read_b128 v[220:223], v162 offset:2048
	ds_read_b128 v[224:227], v162 offset:3072
	ds_read_b128 v[228:231], v162 offset:4096
	ds_read_b128 v[232:235], v162 offset:5120
	ds_read_b128 v[236:239], v162 offset:6144
	ds_read_b128 v[240:243], v162 offset:7168
	global_load_lds_dwordx4 v[144:145], off
	v_lshl_add_u64 v[144:145], s[54:55], 0, v[142:143]
	s_add_i32 m0, s60, 0xe000
	s_nop 0
	global_load_lds_dwordx4 v[144:145], off
	s_waitcnt vmcnt(24)
	s_waitcnt lgkmcnt(0)
	s_barrier
	s_setprio 1
	s_waitcnt lgkmcnt(0)
	v_mfma_f32_16x16x32_bf16 v[124:127], v[164:167], v[200:203], v[124:127]
	v_mfma_f32_16x16x32_bf16 v[120:123], v[172:175], v[200:203], v[120:123]
	v_mfma_f32_16x16x32_bf16 v[108:111], v[164:167], v[220:223], v[108:111]
	v_mfma_f32_16x16x32_bf16 v[104:107], v[172:175], v[220:223], v[104:107]
	v_mfma_f32_16x16x32_bf16 v[92:95], v[164:167], v[228:231], v[92:95]
	v_mfma_f32_16x16x32_bf16 v[88:91], v[172:175], v[228:231], v[88:91]
	v_mfma_f32_16x16x32_bf16 v[76:79], v[164:167], v[236:239], v[76:79]
	v_mfma_f32_16x16x32_bf16 v[72:75], v[172:175], v[236:239], v[72:75]
	v_mfma_f32_16x16x32_bf16 v[124:127], v[168:171], v[216:219], v[124:127]
	v_mfma_f32_16x16x32_bf16 v[120:123], v[176:179], v[216:219], v[120:123]
	v_mfma_f32_16x16x32_bf16 v[108:111], v[168:171], v[224:227], v[108:111]
	v_mfma_f32_16x16x32_bf16 v[104:107], v[176:179], v[224:227], v[104:107]
	v_mfma_f32_16x16x32_bf16 v[92:95], v[168:171], v[232:235], v[92:95]
	v_mfma_f32_16x16x32_bf16 v[88:91], v[176:179], v[232:235], v[88:91]
	v_mfma_f32_16x16x32_bf16 v[76:79], v[168:171], v[240:243], v[76:79]
	v_mfma_f32_16x16x32_bf16 v[72:75], v[176:179], v[240:243], v[72:75]
	s_setprio 0
	s_setprio 1
	v_mfma_f32_16x16x32_bf16 v[116:119], v[180:183], v[200:203], v[116:119]
	v_mfma_f32_16x16x32_bf16 v[112:115], v[188:191], v[200:203], v[112:115]
	v_mfma_f32_16x16x32_bf16 v[100:103], v[180:183], v[220:223], v[100:103]
	v_mfma_f32_16x16x32_bf16 v[96:99], v[188:191], v[220:223], v[96:99]
	v_mfma_f32_16x16x32_bf16 v[84:87], v[180:183], v[228:231], v[84:87]
	v_mfma_f32_16x16x32_bf16 v[80:83], v[188:191], v[228:231], v[80:83]
	v_mfma_f32_16x16x32_bf16 v[68:71], v[180:183], v[236:239], v[68:71]
	v_mfma_f32_16x16x32_bf16 v[64:67], v[188:191], v[236:239], v[64:67]
	v_mfma_f32_16x16x32_bf16 v[116:119], v[184:187], v[216:219], v[116:119]
	v_mfma_f32_16x16x32_bf16 v[112:115], v[192:195], v[216:219], v[112:115]
	v_mfma_f32_16x16x32_bf16 v[100:103], v[184:187], v[224:227], v[100:103]
	v_mfma_f32_16x16x32_bf16 v[96:99], v[192:195], v[224:227], v[96:99]
	v_mfma_f32_16x16x32_bf16 v[84:87], v[184:187], v[232:235], v[84:87]
	v_mfma_f32_16x16x32_bf16 v[80:83], v[192:195], v[232:235], v[80:83]
	v_mfma_f32_16x16x32_bf16 v[68:71], v[184:187], v[240:243], v[68:71]
	v_mfma_f32_16x16x32_bf16 v[64:67], v[192:195], v[240:243], v[64:67]
	s_setprio 0
	s_barrier
	s_add_i32 s71, s71, s33
	v_lshl_add_u64 v[144:145], s[56:57], 0, v[128:129]
	s_mov_b32 m0, s71
	ds_read_b128 v[200:203], v162 offset:16384
	ds_read_b128 v[216:219], v162 offset:17408
	ds_read_b128 v[220:223], v162 offset:18432
	ds_read_b128 v[224:227], v162 offset:19456
	ds_read_b128 v[228:231], v162 offset:20480
	ds_read_b128 v[232:235], v162 offset:21504
	ds_read_b128 v[236:239], v162 offset:22528
	ds_read_b128 v[240:243], v162 offset:23552
	global_load_lds_dwordx4 v[144:145], off
	s_add_i32 m0, s71, 0x2000
	s_add_u32 s72, s56, 0x40000
	v_lshl_add_u64 v[196:197], s[56:57], 0, v[134:135]
	s_addc_u32 s73, s57, 0
	s_add_i32 s71, s76, s33
	global_load_lds_dwordx4 v[196:197], off
	v_lshl_add_u64 v[204:205], s[72:73], 0, v[128:129]
	s_mov_b32 m0, s71
	v_lshl_add_u64 v[206:207], s[58:59], 0, v[132:133]
	global_load_lds_dwordx4 v[204:205], off
	v_lshl_add_u64 v[204:205], s[72:73], 0, v[134:135]
	s_add_i32 m0, s71, 0x2000
	s_nop 0
	global_load_lds_dwordx4 v[204:205], off
	v_lshl_add_u64 v[204:205], s[58:59], 0, v[130:131]
	s_mov_b32 m0, s60
	s_nop 0
	global_load_lds_dwordx4 v[204:205], off
	s_mov_b32 m0, s61
	s_nop 0
	global_load_lds_dwordx4 v[206:207], off
	s_waitcnt vmcnt(24)
	s_waitcnt lgkmcnt(0)
	s_barrier
	s_setprio 1
	s_waitcnt lgkmcnt(0)
	v_mfma_f32_16x16x32_bf16 v[60:63], v[164:167], v[200:203], v[60:63]
	v_mfma_f32_16x16x32_bf16 v[56:59], v[172:175], v[200:203], v[56:59]
	v_mfma_f32_16x16x32_bf16 v[44:47], v[164:167], v[220:223], v[44:47]
	v_mfma_f32_16x16x32_bf16 v[40:43], v[172:175], v[220:223], v[40:43]
	v_mfma_f32_16x16x32_bf16 v[28:31], v[164:167], v[228:231], v[28:31]
	v_mfma_f32_16x16x32_bf16 v[24:27], v[172:175], v[228:231], v[24:27]
	v_mfma_f32_16x16x32_bf16 v[12:15], v[164:167], v[236:239], v[12:15]
	v_mfma_f32_16x16x32_bf16 v[8:11], v[172:175], v[236:239], v[8:11]
	v_mfma_f32_16x16x32_bf16 v[60:63], v[168:171], v[216:219], v[60:63]
	v_mfma_f32_16x16x32_bf16 v[56:59], v[176:179], v[216:219], v[56:59]
	v_mfma_f32_16x16x32_bf16 v[44:47], v[168:171], v[224:227], v[44:47]
	v_mfma_f32_16x16x32_bf16 v[40:43], v[176:179], v[224:227], v[40:43]
	v_mfma_f32_16x16x32_bf16 v[28:31], v[168:171], v[232:235], v[28:31]
	v_mfma_f32_16x16x32_bf16 v[24:27], v[176:179], v[232:235], v[24:27]
	v_mfma_f32_16x16x32_bf16 v[12:15], v[168:171], v[240:243], v[12:15]
	v_mfma_f32_16x16x32_bf16 v[8:11], v[176:179], v[240:243], v[8:11]
	s_setprio 0
	s_setprio 1
	v_mfma_f32_16x16x32_bf16 v[52:55], v[180:183], v[200:203], v[52:55]
	v_mfma_f32_16x16x32_bf16 v[48:51], v[188:191], v[200:203], v[48:51]
	v_mfma_f32_16x16x32_bf16 v[36:39], v[180:183], v[220:223], v[36:39]
	v_mfma_f32_16x16x32_bf16 v[32:35], v[188:191], v[220:223], v[32:35]
	v_mfma_f32_16x16x32_bf16 v[20:23], v[180:183], v[228:231], v[20:23]
	v_mfma_f32_16x16x32_bf16 v[16:19], v[188:191], v[228:231], v[16:19]
	v_mfma_f32_16x16x32_bf16 v[4:7], v[180:183], v[236:239], v[4:7]
	v_mfma_f32_16x16x32_bf16 v[0:3], v[188:191], v[236:239], v[0:3]
	v_mfma_f32_16x16x32_bf16 v[52:55], v[184:187], v[216:219], v[52:55]
	v_mfma_f32_16x16x32_bf16 v[48:51], v[192:195], v[216:219], v[48:51]
	v_mfma_f32_16x16x32_bf16 v[36:39], v[184:187], v[224:227], v[36:39]
	v_mfma_f32_16x16x32_bf16 v[32:35], v[192:195], v[224:227], v[32:35]
	v_mfma_f32_16x16x32_bf16 v[20:23], v[184:187], v[232:235], v[20:23]
	v_mfma_f32_16x16x32_bf16 v[16:19], v[192:195], v[232:235], v[16:19]
	v_mfma_f32_16x16x32_bf16 v[4:7], v[184:187], v[240:243], v[4:7]
	v_mfma_f32_16x16x32_bf16 v[0:3], v[192:195], v[240:243], v[0:3]
	s_setprio 0
	s_barrier
	s_branch .Lp1e_mid

.Lp1e_mid:
	s_add_i32 s71, 0, 0x18000
	v_add_u32_e32 v163, s71, v158
	s_add_i32 s72, 0, 0x1c000
	ds_read_b128 v[164:167], v163
	ds_read_b128 v[168:171], v163 offset:1024
	ds_read_b128 v[172:175], v163 offset:2048
	ds_read_b128 v[176:179], v163 offset:3072
	v_add_u32_e32 v163, s72, v158
	ds_read_b128 v[180:183], v163
	ds_read_b128 v[184:187], v163 offset:1024
	ds_read_b128 v[188:191], v163 offset:2048
	ds_read_b128 v[192:195], v163 offset:3072
	s_add_u32 s58, s58, 0x40000
	s_addc_u32 s59, s59, 0
	s_mov_b32 m0, s62
	v_lshl_add_u64 v[244:245], s[58:59], 0, v[130:131]
	ds_read_b128 v[200:203], v162 offset:32768
	ds_read_b128 v[216:219], v162 offset:33792
	ds_read_b128 v[220:223], v162 offset:34816
	ds_read_b128 v[224:227], v162 offset:35840
	ds_read_b128 v[228:231], v162 offset:36864
	ds_read_b128 v[232:235], v162 offset:37888
	ds_read_b128 v[236:239], v162 offset:38912
	ds_read_b128 v[240:243], v162 offset:39936
	global_load_lds_dwordx4 v[244:245], off
	v_lshl_add_u64 v[244:245], s[58:59], 0, v[132:133]
	s_mov_b32 m0, s63
	s_nop 0
	global_load_lds_dwordx4 v[244:245], off
	s_waitcnt vmcnt(8)
	s_waitcnt lgkmcnt(0)
	s_barrier
	s_setprio 1
	s_waitcnt lgkmcnt(0)
	v_mfma_f32_16x16x32_bf16 v[124:127], v[164:167], v[200:203], v[124:127]
	v_mfma_f32_16x16x32_bf16 v[120:123], v[172:175], v[200:203], v[120:123]
	v_mfma_f32_16x16x32_bf16 v[108:111], v[164:167], v[220:223], v[108:111]
	v_mfma_f32_16x16x32_bf16 v[104:107], v[172:175], v[220:223], v[104:107]
	v_mfma_f32_16x16x32_bf16 v[92:95], v[164:167], v[228:231], v[92:95]
	v_mfma_f32_16x16x32_bf16 v[88:91], v[172:175], v[228:231], v[88:91]
	v_mfma_f32_16x16x32_bf16 v[76:79], v[164:167], v[236:239], v[76:79]
	v_mfma_f32_16x16x32_bf16 v[72:75], v[172:175], v[236:239], v[72:75]
	v_mfma_f32_16x16x32_bf16 v[124:127], v[168:171], v[216:219], v[124:127]
	v_mfma_f32_16x16x32_bf16 v[120:123], v[176:179], v[216:219], v[120:123]
	v_mfma_f32_16x16x32_bf16 v[108:111], v[168:171], v[224:227], v[108:111]
	v_mfma_f32_16x16x32_bf16 v[104:107], v[176:179], v[224:227], v[104:107]
	v_mfma_f32_16x16x32_bf16 v[92:95], v[168:171], v[232:235], v[92:95]
	v_mfma_f32_16x16x32_bf16 v[88:91], v[176:179], v[232:235], v[88:91]
	v_mfma_f32_16x16x32_bf16 v[76:79], v[168:171], v[240:243], v[76:79]
	v_mfma_f32_16x16x32_bf16 v[72:75], v[176:179], v[240:243], v[72:75]
	s_setprio 0
	s_setprio 1
	v_mfma_f32_16x16x32_bf16 v[116:119], v[180:183], v[200:203], v[116:119]
	v_mfma_f32_16x16x32_bf16 v[112:115], v[188:191], v[200:203], v[112:115]
	v_mfma_f32_16x16x32_bf16 v[100:103], v[180:183], v[220:223], v[100:103]
	v_mfma_f32_16x16x32_bf16 v[96:99], v[188:191], v[220:223], v[96:99]
	v_mfma_f32_16x16x32_bf16 v[84:87], v[180:183], v[228:231], v[84:87]
	v_mfma_f32_16x16x32_bf16 v[80:83], v[188:191], v[228:231], v[80:83]
	v_mfma_f32_16x16x32_bf16 v[68:71], v[180:183], v[236:239], v[68:71]
	v_mfma_f32_16x16x32_bf16 v[64:67], v[188:191], v[236:239], v[64:67]
	v_mfma_f32_16x16x32_bf16 v[116:119], v[184:187], v[216:219], v[116:119]
	v_mfma_f32_16x16x32_bf16 v[112:115], v[192:195], v[216:219], v[112:115]
	v_mfma_f32_16x16x32_bf16 v[100:103], v[184:187], v[224:227], v[100:103]
	v_mfma_f32_16x16x32_bf16 v[96:99], v[192:195], v[224:227], v[96:99]
	v_mfma_f32_16x16x32_bf16 v[84:87], v[184:187], v[232:235], v[84:87]
	v_mfma_f32_16x16x32_bf16 v[80:83], v[192:195], v[232:235], v[80:83]
	v_mfma_f32_16x16x32_bf16 v[68:71], v[184:187], v[240:243], v[68:71]
	v_mfma_f32_16x16x32_bf16 v[64:67], v[192:195], v[240:243], v[64:67]
	s_setprio 0
	s_barrier
	s_add_i32 s58, s71, s33
	v_lshl_add_u64 v[144:145], v[144:145], 0, s[88:89]
	s_mov_b32 m0, s58
	ds_read_b128 v[200:203], v162 offset:49152
	ds_read_b128 v[216:219], v162 offset:50176
	ds_read_b128 v[220:223], v162 offset:51200
	ds_read_b128 v[224:227], v162 offset:52224
	ds_read_b128 v[228:231], v162 offset:53248
	ds_read_b128 v[232:235], v162 offset:54272
	ds_read_b128 v[236:239], v162 offset:55296
	ds_read_b128 v[240:243], v162 offset:56320
	global_load_lds_dwordx4 v[144:145], off
	s_add_i32 m0, s58, 0x2000
	s_add_u32 s56, s56, 0x40080
	v_lshl_add_u64 v[144:145], v[196:197], 0, s[88:89]
	s_addc_u32 s57, s57, 0
	s_add_i32 s58, s72, s33
	global_load_lds_dwordx4 v[144:145], off
	v_lshl_add_u64 v[144:145], s[56:57], 0, v[128:129]
	s_mov_b32 m0, s58
	s_nop 0
	global_load_lds_dwordx4 v[144:145], off
	v_lshl_add_u64 v[144:145], s[56:57], 0, v[134:135]
	s_add_i32 m0, s58, 0x2000
	s_nop 0
	global_load_lds_dwordx4 v[144:145], off
	v_lshl_add_u64 v[144:145], v[204:205], 0, s[88:89]
	s_mov_b32 m0, s64
	s_nop 0
	global_load_lds_dwordx4 v[144:145], off
	v_lshl_add_u64 v[144:145], v[206:207], 0, s[88:89]
	s_mov_b32 m0, s65
	s_nop 0
	global_load_lds_dwordx4 v[144:145], off
	s_waitcnt vmcnt(8)
	s_waitcnt lgkmcnt(0)
	s_barrier
	s_setprio 1
	s_waitcnt lgkmcnt(0)
	v_mfma_f32_16x16x32_bf16 v[60:63], v[164:167], v[200:203], v[60:63]
	v_mfma_f32_16x16x32_bf16 v[56:59], v[172:175], v[200:203], v[56:59]
	v_mfma_f32_16x16x32_bf16 v[44:47], v[164:167], v[220:223], v[44:47]
	v_mfma_f32_16x16x32_bf16 v[40:43], v[172:175], v[220:223], v[40:43]
	v_mfma_f32_16x16x32_bf16 v[28:31], v[164:167], v[228:231], v[28:31]
	v_mfma_f32_16x16x32_bf16 v[24:27], v[172:175], v[228:231], v[24:27]
	v_mfma_f32_16x16x32_bf16 v[12:15], v[164:167], v[236:239], v[12:15]
	v_mfma_f32_16x16x32_bf16 v[8:11], v[172:175], v[236:239], v[8:11]
	v_mfma_f32_16x16x32_bf16 v[60:63], v[168:171], v[216:219], v[60:63]
	v_mfma_f32_16x16x32_bf16 v[56:59], v[176:179], v[216:219], v[56:59]
	v_mfma_f32_16x16x32_bf16 v[44:47], v[168:171], v[224:227], v[44:47]
	v_mfma_f32_16x16x32_bf16 v[40:43], v[176:179], v[224:227], v[40:43]
	v_mfma_f32_16x16x32_bf16 v[28:31], v[168:171], v[232:235], v[28:31]
	v_mfma_f32_16x16x32_bf16 v[24:27], v[176:179], v[232:235], v[24:27]
	v_mfma_f32_16x16x32_bf16 v[12:15], v[168:171], v[240:243], v[12:15]
	v_mfma_f32_16x16x32_bf16 v[8:11], v[176:179], v[240:243], v[8:11]
	s_setprio 0
	s_setprio 1
	v_mfma_f32_16x16x32_bf16 v[52:55], v[180:183], v[200:203], v[52:55]
	v_mfma_f32_16x16x32_bf16 v[48:51], v[188:191], v[200:203], v[48:51]
	v_mfma_f32_16x16x32_bf16 v[36:39], v[180:183], v[220:223], v[36:39]
	v_mfma_f32_16x16x32_bf16 v[32:35], v[188:191], v[220:223], v[32:35]
	v_mfma_f32_16x16x32_bf16 v[20:23], v[180:183], v[228:231], v[20:23]
	v_mfma_f32_16x16x32_bf16 v[16:19], v[188:191], v[228:231], v[16:19]
	v_mfma_f32_16x16x32_bf16 v[4:7], v[180:183], v[236:239], v[4:7]
	v_mfma_f32_16x16x32_bf16 v[0:3], v[188:191], v[236:239], v[0:3]
	v_mfma_f32_16x16x32_bf16 v[52:55], v[184:187], v[216:219], v[52:55]
	v_mfma_f32_16x16x32_bf16 v[48:51], v[192:195], v[216:219], v[48:51]
	v_mfma_f32_16x16x32_bf16 v[36:39], v[184:187], v[224:227], v[36:39]
	v_mfma_f32_16x16x32_bf16 v[32:35], v[192:195], v[224:227], v[32:35]
	v_mfma_f32_16x16x32_bf16 v[20:23], v[184:187], v[232:235], v[20:23]
	v_mfma_f32_16x16x32_bf16 v[16:19], v[192:195], v[232:235], v[16:19]
	v_mfma_f32_16x16x32_bf16 v[4:7], v[184:187], v[240:243], v[4:7]
	v_mfma_f32_16x16x32_bf16 v[0:3], v[192:195], v[240:243], v[0:3]
	s_setprio 0
	s_barrier
	s_add_i32 s70, s70, 2
	s_add_u32 s54, s54, 0x100
	s_addc_u32 s55, s55, 0
	s_add_u32 s68, s68, 0x100
	s_addc_u32 s69, s69, 0
	s_cmp_gt_u32 s70, 13
	s_cbranch_scc0 .LBB0_271
	s_and_b64 vcc, exec, s[22:23]
	s_cbranch_vccz .LBB0_274
	s_barrier

.LBB0_294:
	s_or_b64 exec, exec, s[48:49]
	s_ashr_i32 s27, s26, 31
	s_lshl_b64 s[48:49], s[26:27], 19
	s_add_u32 s48, s80, s48
	s_addc_u32 s49, s81, s49
	s_and_b64 s[50:51], s[46:47], exec
	s_cselect_b32 s27, s49, s55
	s_cselect_b32 s53, s48, s54
	s_ashr_i32 s31, s30, 31
	s_lshl_b64 s[50:51], s[30:31], 19
	s_add_u32 s50, s1, s50
	s_addc_u32 s51, s0, s51
	s_and_b64 s[58:59], s[46:47], exec
	s_cselect_b32 s31, s51, s57
	s_cselect_b32 s67, s50, s56
	s_add_u32 s54, s54, 0x40080
	s_addc_u32 s55, s55, 0
	s_add_u32 s68, s56, 0x100
	v_mov_b32_e32 v0, 0
	s_addc_u32 s69, s57, 0
	s_mov_b32 s70, -2
	v_mov_b32_e32 v1, v0
	v_mov_b32_e32 v2, v0
	v_mov_b32_e32 v3, v0
	v_mov_b32_e32 v4, v0
	v_mov_b32_e32 v5, v0
	v_mov_b32_e32 v6, v0
	v_mov_b32_e32 v7, v0
	v_mov_b32_e32 v16, v0
	v_mov_b32_e32 v17, v0
	v_mov_b32_e32 v18, v0
	v_mov_b32_e32 v19, v0
	v_mov_b32_e32 v20, v0
	v_mov_b32_e32 v21, v0
	v_mov_b32_e32 v22, v0
	v_mov_b32_e32 v23, v0
	v_mov_b32_e32 v32, v0
	v_mov_b32_e32 v33, v0
	v_mov_b32_e32 v34, v0
	v_mov_b32_e32 v35, v0
	v_mov_b32_e32 v36, v0
	v_mov_b32_e32 v37, v0
	v_mov_b32_e32 v38, v0
	v_mov_b32_e32 v39, v0
	v_mov_b32_e32 v48, v0
	v_mov_b32_e32 v49, v0
	v_mov_b32_e32 v50, v0
	v_mov_b32_e32 v51, v0
	v_mov_b32_e32 v52, v0
	v_mov_b32_e32 v53, v0
	v_mov_b32_e32 v54, v0
	v_mov_b32_e32 v55, v0
	v_mov_b32_e32 v8, v0
	v_mov_b32_e32 v9, v0
	v_mov_b32_e32 v10, v0
	v_mov_b32_e32 v11, v0
	v_mov_b32_e32 v12, v0
	v_mov_b32_e32 v13, v0
	v_mov_b32_e32 v14, v0
	v_mov_b32_e32 v15, v0
	v_mov_b32_e32 v24, v0
	v_mov_b32_e32 v25, v0
	v_mov_b32_e32 v26, v0
	v_mov_b32_e32 v27, v0
	v_mov_b32_e32 v28, v0
	v_mov_b32_e32 v29, v0
	v_mov_b32_e32 v30, v0
	v_mov_b32_e32 v31, v0
	v_mov_b32_e32 v40, v0
	v_mov_b32_e32 v41, v0
	v_mov_b32_e32 v42, v0
	v_mov_b32_e32 v43, v0
	v_mov_b32_e32 v44, v0
	v_mov_b32_e32 v45, v0
	v_mov_b32_e32 v46, v0
	v_mov_b32_e32 v47, v0
	v_mov_b32_e32 v56, v0
	v_mov_b32_e32 v57, v0
	v_mov_b32_e32 v58, v0
	v_mov_b32_e32 v59, v0
	v_mov_b32_e32 v60, v0
	v_mov_b32_e32 v61, v0
	v_mov_b32_e32 v62, v0
	v_mov_b32_e32 v63, v0
	v_mov_b32_e32 v64, v0
	v_mov_b32_e32 v65, v0
	v_mov_b32_e32 v66, v0
	v_mov_b32_e32 v67, v0
	v_mov_b32_e32 v68, v0
	v_mov_b32_e32 v69, v0
	v_mov_b32_e32 v70, v0
	v_mov_b32_e32 v71, v0
	v_mov_b32_e32 v80, v0
	v_mov_b32_e32 v81, v0
	v_mov_b32_e32 v82, v0
	v_mov_b32_e32 v83, v0
	v_mov_b32_e32 v84, v0
	v_mov_b32_e32 v85, v0
	v_mov_b32_e32 v86, v0
	v_mov_b32_e32 v87, v0
	v_mov_b32_e32 v96, v0
	v_mov_b32_e32 v97, v0
	v_mov_b32_e32 v98, v0
	v_mov_b32_e32 v99, v0
	v_mov_b32_e32 v100, v0
	v_mov_b32_e32 v101, v0
	v_mov_b32_e32 v102, v0
	v_mov_b32_e32 v103, v0
	v_mov_b32_e32 v112, v0
	v_mov_b32_e32 v113, v0
	v_mov_b32_e32 v114, v0
	v_mov_b32_e32 v115, v0
	v_mov_b32_e32 v116, v0
	v_mov_b32_e32 v117, v0
	v_mov_b32_e32 v118, v0
	v_mov_b32_e32 v119, v0
	v_mov_b32_e32 v72, v0
	v_mov_b32_e32 v73, v0
	v_mov_b32_e32 v74, v0
	v_mov_b32_e32 v75, v0
	v_mov_b32_e32 v76, v0
	v_mov_b32_e32 v77, v0
	v_mov_b32_e32 v78, v0
	v_mov_b32_e32 v79, v0
	v_mov_b32_e32 v88, v0
	v_mov_b32_e32 v89, v0
	v_mov_b32_e32 v90, v0
	v_mov_b32_e32 v91, v0
	v_mov_b32_e32 v92, v0
	v_mov_b32_e32 v93, v0
	v_mov_b32_e32 v94, v0
	v_mov_b32_e32 v95, v0
	v_mov_b32_e32 v104, v0
	v_mov_b32_e32 v105, v0
	v_mov_b32_e32 v106, v0
	v_mov_b32_e32 v107, v0
	v_mov_b32_e32 v108, v0
	v_mov_b32_e32 v109, v0
	v_mov_b32_e32 v110, v0
	v_mov_b32_e32 v111, v0
	v_mov_b32_e32 v120, v0
	v_mov_b32_e32 v121, v0
	v_mov_b32_e32 v122, v0
	v_mov_b32_e32 v123, v0
	v_mov_b32_e32 v124, v0
	v_mov_b32_e32 v125, v0
	v_mov_b32_e32 v126, v0
	v_mov_b32_e32 v127, v0
	s_cmp_eq_u32 s9, 0
	s_cbranch_scc1 .LBB0_295
	s_add_u32 s56, s54, 0xfffc0080
	s_addc_u32 s57, s55, -1
	s_add_i32 s71, 0, 0x10000
	s_cmp_eq_u32 s70, 12
	s_cselect_b32 s59, s27, s57
	s_cselect_b32 s58, s53, s56
	v_add_u32_e32 v144, s71, v158
	s_cselect_b32 s57, s31, s69
	s_cselect_b32 s56, s67, s68
	s_add_i32 s76, 0, 0x14000
	ds_read_b128 v[162:165], v144
	ds_read_b128 v[166:169], v144 offset:1024
	ds_read_b128 v[170:173], v144 offset:2048
	ds_read_b128 v[174:177], v144 offset:3072
	v_add_u32_e32 v144, s76, v158
	ds_read_b128 v[178:181], v144
	ds_read_b128 v[182:185], v144 offset:1024
	ds_read_b128 v[186:189], v144 offset:2048
	ds_read_b128 v[190:193], v144 offset:3072
	v_lshl_add_u64 v[144:145], s[54:55], 0, v[140:141]
	s_add_i32 m0, s60, 0xc000
	ds_read_b128 v[194:197], v160
	ds_read_b128 v[200:203], v160 offset:1024
	ds_read_b128 v[216:219], v160 offset:2048
	ds_read_b128 v[220:223], v160 offset:3072
	ds_read_b128 v[224:227], v160 offset:4096
	ds_read_b128 v[228:231], v160 offset:5120
	ds_read_b128 v[232:235], v160 offset:6144
	ds_read_b128 v[236:239], v160 offset:7168
	global_load_lds_dwordx4 v[144:145], off
	v_lshl_add_u64 v[144:145], s[54:55], 0, v[142:143]
	s_add_i32 m0, s60, 0xe000
	s_nop 0
	global_load_lds_dwordx4 v[144:145], off
	s_waitcnt vmcnt(24)
	s_waitcnt lgkmcnt(0)
	s_barrier
	s_setprio 1
	s_waitcnt lgkmcnt(0)
	v_mfma_f32_16x16x32_bf16 v[124:127], v[162:165], v[194:197], v[124:127]
	v_mfma_f32_16x16x32_bf16 v[120:123], v[170:173], v[194:197], v[120:123]
	v_mfma_f32_16x16x32_bf16 v[108:111], v[162:165], v[216:219], v[108:111]
	v_mfma_f32_16x16x32_bf16 v[104:107], v[170:173], v[216:219], v[104:107]
	v_mfma_f32_16x16x32_bf16 v[92:95], v[162:165], v[224:227], v[92:95]
	v_mfma_f32_16x16x32_bf16 v[88:91], v[170:173], v[224:227], v[88:91]
	v_mfma_f32_16x16x32_bf16 v[76:79], v[162:165], v[232:235], v[76:79]
	v_mfma_f32_16x16x32_bf16 v[72:75], v[170:173], v[232:235], v[72:75]
	v_mfma_f32_16x16x32_bf16 v[124:127], v[166:169], v[200:203], v[124:127]
	v_mfma_f32_16x16x32_bf16 v[120:123], v[174:177], v[200:203], v[120:123]
	v_mfma_f32_16x16x32_bf16 v[108:111], v[166:169], v[220:223], v[108:111]
	v_mfma_f32_16x16x32_bf16 v[104:107], v[174:177], v[220:223], v[104:107]
	v_mfma_f32_16x16x32_bf16 v[92:95], v[166:169], v[228:231], v[92:95]
	v_mfma_f32_16x16x32_bf16 v[88:91], v[174:177], v[228:231], v[88:91]
	v_mfma_f32_16x16x32_bf16 v[76:79], v[166:169], v[236:239], v[76:79]
	v_mfma_f32_16x16x32_bf16 v[72:75], v[174:177], v[236:239], v[72:75]
	s_setprio 0
	s_setprio 1
	v_mfma_f32_16x16x32_bf16 v[116:119], v[178:181], v[194:197], v[116:119]
	v_mfma_f32_16x16x32_bf16 v[112:115], v[186:189], v[194:197], v[112:115]
	v_mfma_f32_16x16x32_bf16 v[100:103], v[178:181], v[216:219], v[100:103]
	v_mfma_f32_16x16x32_bf16 v[96:99], v[186:189], v[216:219], v[96:99]
	v_mfma_f32_16x16x32_bf16 v[84:87], v[178:181], v[224:227], v[84:87]
	v_mfma_f32_16x16x32_bf16 v[80:83], v[186:189], v[224:227], v[80:83]
	v_mfma_f32_16x16x32_bf16 v[68:71], v[178:181], v[232:235], v[68:71]
	v_mfma_f32_16x16x32_bf16 v[64:67], v[186:189], v[232:235], v[64:67]
	v_mfma_f32_16x16x32_bf16 v[116:119], v[182:185], v[200:203], v[116:119]
	v_mfma_f32_16x16x32_bf16 v[112:115], v[190:193], v[200:203], v[112:115]
	v_mfma_f32_16x16x32_bf16 v[100:103], v[182:185], v[220:223], v[100:103]
	v_mfma_f32_16x16x32_bf16 v[96:99], v[190:193], v[220:223], v[96:99]
	v_mfma_f32_16x16x32_bf16 v[84:87], v[182:185], v[228:231], v[84:87]
	v_mfma_f32_16x16x32_bf16 v[80:83], v[190:193], v[228:231], v[80:83]
	v_mfma_f32_16x16x32_bf16 v[68:71], v[182:185], v[236:239], v[68:71]
	v_mfma_f32_16x16x32_bf16 v[64:67], v[190:193], v[236:239], v[64:67]
	s_setprio 0
	s_barrier
	s_add_i32 s71, s71, s33
	v_lshl_add_u64 v[144:145], s[56:57], 0, v[128:129]
	s_mov_b32 m0, s71
	ds_read_b128 v[194:197], v160 offset:16384
	ds_read_b128 v[200:203], v160 offset:17408
	ds_read_b128 v[216:219], v160 offset:18432
	ds_read_b128 v[220:223], v160 offset:19456
	ds_read_b128 v[224:227], v160 offset:20480
	ds_read_b128 v[228:231], v160 offset:21504
	ds_read_b128 v[232:235], v160 offset:22528
	ds_read_b128 v[236:239], v160 offset:23552
	global_load_lds_dwordx4 v[144:145], off
	s_add_i32 m0, s71, 0x2000
	s_add_u32 s72, s56, 0x40000
	v_lshl_add_u64 v[204:205], s[56:57], 0, v[134:135]
	s_addc_u32 s73, s57, 0
	s_add_i32 s71, s76, s33
	global_load_lds_dwordx4 v[204:205], off
	v_lshl_add_u64 v[206:207], s[72:73], 0, v[128:129]
	s_mov_b32 m0, s71
	v_lshl_add_u64 v[240:241], s[58:59], 0, v[132:133]
	global_load_lds_dwordx4 v[206:207], off
	v_lshl_add_u64 v[206:207], s[72:73], 0, v[134:135]
	s_add_i32 m0, s71, 0x2000
	s_nop 0
	global_load_lds_dwordx4 v[206:207], off
	v_lshl_add_u64 v[206:207], s[58:59], 0, v[130:131]
	s_mov_b32 m0, s60
	s_nop 0
	global_load_lds_dwordx4 v[206:207], off
	s_mov_b32 m0, s61
	s_nop 0
	global_load_lds_dwordx4 v[240:241], off
	s_waitcnt vmcnt(24)
	s_waitcnt lgkmcnt(0)
	s_barrier
	s_setprio 1
	s_waitcnt lgkmcnt(0)
	v_mfma_f32_16x16x32_bf16 v[60:63], v[162:165], v[194:197], v[60:63]
	v_mfma_f32_16x16x32_bf16 v[56:59], v[170:173], v[194:197], v[56:59]
	v_mfma_f32_16x16x32_bf16 v[44:47], v[162:165], v[216:219], v[44:47]
	v_mfma_f32_16x16x32_bf16 v[40:43], v[170:173], v[216:219], v[40:43]
	v_mfma_f32_16x16x32_bf16 v[28:31], v[162:165], v[224:227], v[28:31]
	v_mfma_f32_16x16x32_bf16 v[24:27], v[170:173], v[224:227], v[24:27]
	v_mfma_f32_16x16x32_bf16 v[12:15], v[162:165], v[232:235], v[12:15]
	v_mfma_f32_16x16x32_bf16 v[8:11], v[170:173], v[232:235], v[8:11]
	v_mfma_f32_16x16x32_bf16 v[60:63], v[166:169], v[200:203], v[60:63]
	v_mfma_f32_16x16x32_bf16 v[56:59], v[174:177], v[200:203], v[56:59]
	v_mfma_f32_16x16x32_bf16 v[44:47], v[166:169], v[220:223], v[44:47]
	v_mfma_f32_16x16x32_bf16 v[40:43], v[174:177], v[220:223], v[40:43]
	v_mfma_f32_16x16x32_bf16 v[28:31], v[166:169], v[228:231], v[28:31]
	v_mfma_f32_16x16x32_bf16 v[24:27], v[174:177], v[228:231], v[24:27]
	v_mfma_f32_16x16x32_bf16 v[12:15], v[166:169], v[236:239], v[12:15]
	v_mfma_f32_16x16x32_bf16 v[8:11], v[174:177], v[236:239], v[8:11]
	s_setprio 0
	s_setprio 1
	v_mfma_f32_16x16x32_bf16 v[52:55], v[178:181], v[194:197], v[52:55]
	v_mfma_f32_16x16x32_bf16 v[48:51], v[186:189], v[194:197], v[48:51]
	v_mfma_f32_16x16x32_bf16 v[36:39], v[178:181], v[216:219], v[36:39]
	v_mfma_f32_16x16x32_bf16 v[32:35], v[186:189], v[216:219], v[32:35]
	v_mfma_f32_16x16x32_bf16 v[20:23], v[178:181], v[224:227], v[20:23]
	v_mfma_f32_16x16x32_bf16 v[16:19], v[186:189], v[224:227], v[16:19]
	v_mfma_f32_16x16x32_bf16 v[4:7], v[178:181], v[232:235], v[4:7]
	v_mfma_f32_16x16x32_bf16 v[0:3], v[186:189], v[232:235], v[0:3]
	v_mfma_f32_16x16x32_bf16 v[52:55], v[182:185], v[200:203], v[52:55]
	v_mfma_f32_16x16x32_bf16 v[48:51], v[190:193], v[200:203], v[48:51]
	v_mfma_f32_16x16x32_bf16 v[36:39], v[182:185], v[220:223], v[36:39]
	v_mfma_f32_16x16x32_bf16 v[32:35], v[190:193], v[220:223], v[32:35]
	v_mfma_f32_16x16x32_bf16 v[20:23], v[182:185], v[228:231], v[20:23]
	v_mfma_f32_16x16x32_bf16 v[16:19], v[190:193], v[228:231], v[16:19]
	v_mfma_f32_16x16x32_bf16 v[4:7], v[182:185], v[236:239], v[4:7]
	v_mfma_f32_16x16x32_bf16 v[0:3], v[190:193], v[236:239], v[0:3]
	s_setprio 0
	s_barrier
	s_branch .Lp1o_mid

.Lp1o_mid:
	s_add_i32 s71, 0, 0x18000
	v_add_u32_e32 v161, s71, v158
	s_add_i32 s72, 0, 0x1c000
	ds_read_b128 v[162:165], v161
	ds_read_b128 v[166:169], v161 offset:1024
	ds_read_b128 v[170:173], v161 offset:2048
	ds_read_b128 v[174:177], v161 offset:3072
	v_add_u32_e32 v161, s72, v158
	ds_read_b128 v[178:181], v161
	ds_read_b128 v[182:185], v161 offset:1024
	ds_read_b128 v[186:189], v161 offset:2048
	ds_read_b128 v[190:193], v161 offset:3072
	s_add_u32 s58, s58, 0x40000
	s_addc_u32 s59, s59, 0
	s_mov_b32 m0, s62
	v_lshl_add_u64 v[242:243], s[58:59], 0, v[130:131]
	ds_read_b128 v[194:197], v160 offset:32768
	ds_read_b128 v[200:203], v160 offset:33792
	ds_read_b128 v[216:219], v160 offset:34816
	ds_read_b128 v[220:223], v160 offset:35840
	ds_read_b128 v[224:227], v160 offset:36864
	ds_read_b128 v[228:231], v160 offset:37888
	ds_read_b128 v[232:235], v160 offset:38912
	ds_read_b128 v[236:239], v160 offset:39936
	global_load_lds_dwordx4 v[242:243], off
	v_lshl_add_u64 v[242:243], s[58:59], 0, v[132:133]
	s_mov_b32 m0, s63
	s_nop 0
	global_load_lds_dwordx4 v[242:243], off
	s_waitcnt vmcnt(8)
	s_waitcnt lgkmcnt(0)
	s_barrier
	s_setprio 1
	s_waitcnt lgkmcnt(0)
	v_mfma_f32_16x16x32_bf16 v[124:127], v[162:165], v[194:197], v[124:127]
	v_mfma_f32_16x16x32_bf16 v[120:123], v[170:173], v[194:197], v[120:123]
	v_mfma_f32_16x16x32_bf16 v[108:111], v[162:165], v[216:219], v[108:111]
	v_mfma_f32_16x16x32_bf16 v[104:107], v[170:173], v[216:219], v[104:107]
	v_mfma_f32_16x16x32_bf16 v[92:95], v[162:165], v[224:227], v[92:95]
	v_mfma_f32_16x16x32_bf16 v[88:91], v[170:173], v[224:227], v[88:91]
	v_mfma_f32_16x16x32_bf16 v[76:79], v[162:165], v[232:235], v[76:79]
	v_mfma_f32_16x16x32_bf16 v[72:75], v[170:173], v[232:235], v[72:75]
	v_mfma_f32_16x16x32_bf16 v[124:127], v[166:169], v[200:203], v[124:127]
	v_mfma_f32_16x16x32_bf16 v[120:123], v[174:177], v[200:203], v[120:123]
	v_mfma_f32_16x16x32_bf16 v[108:111], v[166:169], v[220:223], v[108:111]
	v_mfma_f32_16x16x32_bf16 v[104:107], v[174:177], v[220:223], v[104:107]
	v_mfma_f32_16x16x32_bf16 v[92:95], v[166:169], v[228:231], v[92:95]
	v_mfma_f32_16x16x32_bf16 v[88:91], v[174:177], v[228:231], v[88:91]
	v_mfma_f32_16x16x32_bf16 v[76:79], v[166:169], v[236:239], v[76:79]
	v_mfma_f32_16x16x32_bf16 v[72:75], v[174:177], v[236:239], v[72:75]
	s_setprio 0
	s_setprio 1
	v_mfma_f32_16x16x32_bf16 v[116:119], v[178:181], v[194:197], v[116:119]
	v_mfma_f32_16x16x32_bf16 v[112:115], v[186:189], v[194:197], v[112:115]
	v_mfma_f32_16x16x32_bf16 v[100:103], v[178:181], v[216:219], v[100:103]
	v_mfma_f32_16x16x32_bf16 v[96:99], v[186:189], v[216:219], v[96:99]
	v_mfma_f32_16x16x32_bf16 v[84:87], v[178:181], v[224:227], v[84:87]
	v_mfma_f32_16x16x32_bf16 v[80:83], v[186:189], v[224:227], v[80:83]
	v_mfma_f32_16x16x32_bf16 v[68:71], v[178:181], v[232:235], v[68:71]
	v_mfma_f32_16x16x32_bf16 v[64:67], v[186:189], v[232:235], v[64:67]
	v_mfma_f32_16x16x32_bf16 v[116:119], v[182:185], v[200:203], v[116:119]
	v_mfma_f32_16x16x32_bf16 v[112:115], v[190:193], v[200:203], v[112:115]
	v_mfma_f32_16x16x32_bf16 v[100:103], v[182:185], v[220:223], v[100:103]
	v_mfma_f32_16x16x32_bf16 v[96:99], v[190:193], v[220:223], v[96:99]
	v_mfma_f32_16x16x32_bf16 v[84:87], v[182:185], v[228:231], v[84:87]
	v_mfma_f32_16x16x32_bf16 v[80:83], v[190:193], v[228:231], v[80:83]
	v_mfma_f32_16x16x32_bf16 v[68:71], v[182:185], v[236:239], v[68:71]
	v_mfma_f32_16x16x32_bf16 v[64:67], v[190:193], v[236:239], v[64:67]
	s_setprio 0
	s_barrier
	s_add_i32 s58, s71, s33
	v_lshl_add_u64 v[144:145], v[144:145], 0, s[88:89]
	s_mov_b32 m0, s58
	ds_read_b128 v[194:197], v160 offset:49152
	ds_read_b128 v[200:203], v160 offset:50176
	ds_read_b128 v[216:219], v160 offset:51200
	ds_read_b128 v[220:223], v160 offset:52224
	ds_read_b128 v[224:227], v160 offset:53248
	ds_read_b128 v[228:231], v160 offset:54272
	ds_read_b128 v[232:235], v160 offset:55296
	ds_read_b128 v[236:239], v160 offset:56320
	global_load_lds_dwordx4 v[144:145], off
	s_add_i32 m0, s58, 0x2000
	s_add_u32 s56, s56, 0x40080
	v_lshl_add_u64 v[144:145], v[204:205], 0, s[88:89]
	s_addc_u32 s57, s57, 0
	s_add_i32 s58, s72, s33
	global_load_lds_dwordx4 v[144:145], off
	v_lshl_add_u64 v[144:145], s[56:57], 0, v[128:129]
	s_mov_b32 m0, s58
	s_nop 0
	global_load_lds_dwordx4 v[144:145], off
	v_lshl_add_u64 v[144:145], s[56:57], 0, v[134:135]
	s_add_i32 m0, s58, 0x2000
	s_nop 0
	global_load_lds_dwordx4 v[144:145], off
	v_lshl_add_u64 v[144:145], v[206:207], 0, s[88:89]
	s_mov_b32 m0, s64
	s_nop 0
	global_load_lds_dwordx4 v[144:145], off
	v_lshl_add_u64 v[144:145], v[240:241], 0, s[88:89]
	s_mov_b32 m0, s65
	s_nop 0
	global_load_lds_dwordx4 v[144:145], off
	s_waitcnt vmcnt(8)
	s_waitcnt lgkmcnt(0)
	s_barrier
	s_setprio 1
	s_waitcnt lgkmcnt(0)
	v_mfma_f32_16x16x32_bf16 v[60:63], v[162:165], v[194:197], v[60:63]
	v_mfma_f32_16x16x32_bf16 v[56:59], v[170:173], v[194:197], v[56:59]
	v_mfma_f32_16x16x32_bf16 v[44:47], v[162:165], v[216:219], v[44:47]
	v_mfma_f32_16x16x32_bf16 v[40:43], v[170:173], v[216:219], v[40:43]
	v_mfma_f32_16x16x32_bf16 v[28:31], v[162:165], v[224:227], v[28:31]
	v_mfma_f32_16x16x32_bf16 v[24:27], v[170:173], v[224:227], v[24:27]
	v_mfma_f32_16x16x32_bf16 v[12:15], v[162:165], v[232:235], v[12:15]
	v_mfma_f32_16x16x32_bf16 v[8:11], v[170:173], v[232:235], v[8:11]
	v_mfma_f32_16x16x32_bf16 v[60:63], v[166:169], v[200:203], v[60:63]
	v_mfma_f32_16x16x32_bf16 v[56:59], v[174:177], v[200:203], v[56:59]
	v_mfma_f32_16x16x32_bf16 v[44:47], v[166:169], v[220:223], v[44:47]
	v_mfma_f32_16x16x32_bf16 v[40:43], v[174:177], v[220:223], v[40:43]
	v_mfma_f32_16x16x32_bf16 v[28:31], v[166:169], v[228:231], v[28:31]
	v_mfma_f32_16x16x32_bf16 v[24:27], v[174:177], v[228:231], v[24:27]
	v_mfma_f32_16x16x32_bf16 v[12:15], v[166:169], v[236:239], v[12:15]
	v_mfma_f32_16x16x32_bf16 v[8:11], v[174:177], v[236:239], v[8:11]
	s_setprio 0
	s_setprio 1
	v_mfma_f32_16x16x32_bf16 v[52:55], v[178:181], v[194:197], v[52:55]
	v_mfma_f32_16x16x32_bf16 v[48:51], v[186:189], v[194:197], v[48:51]
	v_mfma_f32_16x16x32_bf16 v[36:39], v[178:181], v[216:219], v[36:39]
	v_mfma_f32_16x16x32_bf16 v[32:35], v[186:189], v[216:219], v[32:35]
	v_mfma_f32_16x16x32_bf16 v[20:23], v[178:181], v[224:227], v[20:23]
	v_mfma_f32_16x16x32_bf16 v[16:19], v[186:189], v[224:227], v[16:19]
	v_mfma_f32_16x16x32_bf16 v[4:7], v[178:181], v[232:235], v[4:7]
	v_mfma_f32_16x16x32_bf16 v[0:3], v[186:189], v[232:235], v[0:3]
	v_mfma_f32_16x16x32_bf16 v[52:55], v[182:185], v[200:203], v[52:55]
	v_mfma_f32_16x16x32_bf16 v[48:51], v[190:193], v[200:203], v[48:51]
	v_mfma_f32_16x16x32_bf16 v[36:39], v[182:185], v[220:223], v[36:39]
	v_mfma_f32_16x16x32_bf16 v[32:35], v[190:193], v[220:223], v[32:35]
	v_mfma_f32_16x16x32_bf16 v[20:23], v[182:185], v[228:231], v[20:23]
	v_mfma_f32_16x16x32_bf16 v[16:19], v[190:193], v[228:231], v[16:19]
	v_mfma_f32_16x16x32_bf16 v[4:7], v[182:185], v[236:239], v[4:7]
	v_mfma_f32_16x16x32_bf16 v[0:3], v[190:193], v[236:239], v[0:3]
	s_setprio 0
	s_barrier
	s_add_i32 s70, s70, 2
	s_add_u32 s54, s54, 0x100
	s_addc_u32 s55, s55, 0
	s_add_u32 s68, s68, 0x100
	s_addc_u32 s69, s69, 0
	s_cmp_gt_u32 s70, 13
	s_cbranch_scc0 .LBB0_295
	s_and_b64 vcc, exec, s[22:23]
	s_cbranch_vccz .LBB0_298
	s_barrier

.LBB0_1277:
	s_ashr_i32 s49, s48, 31
	s_lshl_b64 s[8:9], s[48:49], 19
	v_readlane_b32 s50, v251, 4
	v_readlane_b32 s51, v251, 5
	s_add_u32 s50, s50, s8
	s_addc_u32 s51, s51, s9
	s_and_b64 s[8:9], s[58:59], exec
	s_cselect_b32 s8, s51, s55
	s_cselect_b32 s9, s50, s54
	s_ashr_i32 s47, s46, 31
	s_lshl_b64 s[52:53], s[46:47], 19
	v_readlane_b32 s66, v255, 41
	v_readlane_b32 s67, v255, 42
	s_add_u32 s52, s66, s52
	s_addc_u32 s53, s67, s53
	s_and_b64 s[58:59], s[58:59], exec
	s_cselect_b32 s21, s53, s57
	s_cselect_b32 s23, s52, s56
	s_add_u32 s54, s54, 0x40080
	s_addc_u32 s55, s55, 0
	s_add_u32 s27, s56, 0x100
	v_mov_b32_e32 v0, 0
	s_addc_u32 s47, s57, 0
	s_mov_b32 s49, -2
	v_mov_b32_e32 v1, v0
	v_mov_b32_e32 v2, v0
	v_mov_b32_e32 v3, v0
	v_mov_b32_e32 v4, v0
	v_mov_b32_e32 v5, v0
	v_mov_b32_e32 v6, v0
	v_mov_b32_e32 v7, v0
	v_mov_b32_e32 v16, v0
	v_mov_b32_e32 v17, v0
	v_mov_b32_e32 v18, v0
	v_mov_b32_e32 v19, v0
	v_mov_b32_e32 v20, v0
	v_mov_b32_e32 v21, v0
	v_mov_b32_e32 v22, v0
	v_mov_b32_e32 v23, v0
	v_mov_b32_e32 v32, v0
	v_mov_b32_e32 v33, v0
	v_mov_b32_e32 v34, v0
	v_mov_b32_e32 v35, v0
	v_mov_b32_e32 v36, v0
	v_mov_b32_e32 v37, v0
	v_mov_b32_e32 v38, v0
	v_mov_b32_e32 v39, v0
	v_mov_b32_e32 v48, v0
	v_mov_b32_e32 v49, v0
	v_mov_b32_e32 v50, v0
	v_mov_b32_e32 v51, v0
	v_mov_b32_e32 v52, v0
	v_mov_b32_e32 v53, v0
	v_mov_b32_e32 v54, v0
	v_mov_b32_e32 v55, v0
	v_mov_b32_e32 v8, v0
	v_mov_b32_e32 v9, v0
	v_mov_b32_e32 v10, v0
	v_mov_b32_e32 v11, v0
	v_mov_b32_e32 v12, v0
	v_mov_b32_e32 v13, v0
	v_mov_b32_e32 v14, v0
	v_mov_b32_e32 v15, v0
	v_mov_b32_e32 v24, v0
	v_mov_b32_e32 v25, v0
	v_mov_b32_e32 v26, v0
	v_mov_b32_e32 v27, v0
	v_mov_b32_e32 v28, v0
	v_mov_b32_e32 v29, v0
	v_mov_b32_e32 v30, v0
	v_mov_b32_e32 v31, v0
	v_mov_b32_e32 v40, v0
	v_mov_b32_e32 v41, v0
	v_mov_b32_e32 v42, v0
	v_mov_b32_e32 v43, v0
	v_mov_b32_e32 v44, v0
	v_mov_b32_e32 v45, v0
	v_mov_b32_e32 v46, v0
	v_mov_b32_e32 v47, v0
	v_mov_b32_e32 v56, v0
	v_mov_b32_e32 v57, v0
	v_mov_b32_e32 v58, v0
	v_mov_b32_e32 v59, v0
	v_mov_b32_e32 v60, v0
	v_mov_b32_e32 v61, v0
	v_mov_b32_e32 v62, v0
	v_mov_b32_e32 v63, v0
	v_mov_b32_e32 v64, v0
	v_mov_b32_e32 v65, v0
	v_mov_b32_e32 v66, v0
	v_mov_b32_e32 v67, v0
	v_mov_b32_e32 v68, v0
	v_mov_b32_e32 v69, v0
	v_mov_b32_e32 v70, v0
	v_mov_b32_e32 v71, v0
	v_mov_b32_e32 v80, v0
	v_mov_b32_e32 v81, v0
	v_mov_b32_e32 v82, v0
	v_mov_b32_e32 v83, v0
	v_mov_b32_e32 v84, v0
	v_mov_b32_e32 v85, v0
	v_mov_b32_e32 v86, v0
	v_mov_b32_e32 v87, v0
	v_mov_b32_e32 v96, v0
	v_mov_b32_e32 v97, v0
	v_mov_b32_e32 v98, v0
	v_mov_b32_e32 v99, v0
	v_mov_b32_e32 v100, v0
	v_mov_b32_e32 v101, v0
	v_mov_b32_e32 v102, v0
	v_mov_b32_e32 v103, v0
	v_mov_b32_e32 v104, v0
	v_mov_b32_e32 v105, v0
	v_mov_b32_e32 v106, v0
	v_mov_b32_e32 v107, v0
	v_mov_b32_e32 v112, v0
	v_mov_b32_e32 v113, v0
	v_mov_b32_e32 v114, v0
	v_mov_b32_e32 v115, v0
	v_mov_b32_e32 v72, v0
	v_mov_b32_e32 v73, v0
	v_mov_b32_e32 v74, v0
	v_mov_b32_e32 v75, v0
	v_mov_b32_e32 v76, v0
	v_mov_b32_e32 v77, v0
	v_mov_b32_e32 v78, v0
	v_mov_b32_e32 v79, v0
	v_mov_b32_e32 v88, v0
	v_mov_b32_e32 v89, v0
	v_mov_b32_e32 v90, v0
	v_mov_b32_e32 v91, v0
	v_mov_b32_e32 v92, v0
	v_mov_b32_e32 v93, v0
	v_mov_b32_e32 v94, v0
	v_mov_b32_e32 v95, v0
	v_mov_b32_e32 v108, v0
	v_mov_b32_e32 v109, v0
	v_mov_b32_e32 v110, v0
	v_mov_b32_e32 v111, v0
	v_mov_b32_e32 v116, v0
	v_mov_b32_e32 v117, v0
	v_mov_b32_e32 v118, v0
	v_mov_b32_e32 v119, v0
	v_mov_b32_e32 v120, v0
	v_mov_b32_e32 v121, v0
	v_mov_b32_e32 v122, v0
	v_mov_b32_e32 v123, v0
	v_mov_b32_e32 v124, v0
	v_mov_b32_e32 v125, v0
	v_mov_b32_e32 v126, v0
	v_mov_b32_e32 v127, v0
	s_cmp_eq_u32 s64, 1
	s_cbranch_scc1 .LBB0_1278
	s_add_u32 s56, s54, 0xfffc0080
	s_addc_u32 s57, s55, -1
	s_add_i32 s66, 0, 0x10000
	s_cmp_eq_u32 s49, 12
	s_cselect_b32 s59, s8, s57
	s_cselect_b32 s58, s9, s56
	s_cselect_b32 s57, s21, s47
	s_cselect_b32 s56, s23, s27
	s_add_i32 s68, 0, 0x14000
	v_add_u32_e32 v142, s66, v190
	v_add_u32_e32 v170, s68, v190
	ds_read_b128 v[130:133], v142
	ds_read_b128 v[134:137], v142 offset:1024
	ds_read_b128 v[138:141], v142 offset:2048
	ds_read_b128 v[142:145], v142 offset:3072
	ds_read_b128 v[146:149], v170
	ds_read_b128 v[150:153], v170 offset:1024
	ds_read_b128 v[166:169], v170 offset:2048
	ds_read_b128 v[170:173], v170 offset:3072
	v_lshl_add_u64 v[206:207], s[54:55], 0, v[162:163]
	s_add_i32 m0, s1, 0xc000
	ds_read_b128 v[174:177], v197
	ds_read_b128 v[202:205], v197 offset:1024
	ds_read_b128 v[216:219], v197 offset:2048
	ds_read_b128 v[220:223], v197 offset:3072
	ds_read_b128 v[224:227], v197 offset:4096
	ds_read_b128 v[228:231], v197 offset:5120
	ds_read_b128 v[232:235], v197 offset:6144
	ds_read_b128 v[236:239], v197 offset:7168
	global_load_lds_dwordx4 v[206:207], off
	v_lshl_add_u64 v[206:207], s[54:55], 0, v[164:165]
	s_add_i32 m0, s1, 0xe000
	s_nop 0
	global_load_lds_dwordx4 v[206:207], off
	s_waitcnt vmcnt(24)
	s_waitcnt lgkmcnt(0)
	s_barrier
	s_setprio 1
	s_waitcnt lgkmcnt(0)
	v_mfma_f32_16x16x32_bf16 v[124:127], v[130:133], v[174:177], v[124:127]
	v_mfma_f32_16x16x32_bf16 v[120:123], v[138:141], v[174:177], v[120:123]
	v_mfma_f32_16x16x32_bf16 v[116:119], v[130:133], v[216:219], v[116:119]
	v_mfma_f32_16x16x32_bf16 v[108:111], v[138:141], v[216:219], v[108:111]
	v_mfma_f32_16x16x32_bf16 v[92:95], v[130:133], v[224:227], v[92:95]
	v_mfma_f32_16x16x32_bf16 v[88:91], v[138:141], v[224:227], v[88:91]
	v_mfma_f32_16x16x32_bf16 v[76:79], v[130:133], v[232:235], v[76:79]
	v_mfma_f32_16x16x32_bf16 v[72:75], v[138:141], v[232:235], v[72:75]
	v_mfma_f32_16x16x32_bf16 v[124:127], v[134:137], v[202:205], v[124:127]
	v_mfma_f32_16x16x32_bf16 v[120:123], v[142:145], v[202:205], v[120:123]
	v_mfma_f32_16x16x32_bf16 v[116:119], v[134:137], v[220:223], v[116:119]
	v_mfma_f32_16x16x32_bf16 v[108:111], v[142:145], v[220:223], v[108:111]
	v_mfma_f32_16x16x32_bf16 v[92:95], v[134:137], v[228:231], v[92:95]
	v_mfma_f32_16x16x32_bf16 v[88:91], v[142:145], v[228:231], v[88:91]
	v_mfma_f32_16x16x32_bf16 v[76:79], v[134:137], v[236:239], v[76:79]
	v_mfma_f32_16x16x32_bf16 v[72:75], v[142:145], v[236:239], v[72:75]
	s_setprio 0
	s_setprio 1
	v_mfma_f32_16x16x32_bf16 v[112:115], v[146:149], v[174:177], v[112:115]
	v_mfma_f32_16x16x32_bf16 v[104:107], v[166:169], v[174:177], v[104:107]
	v_mfma_f32_16x16x32_bf16 v[100:103], v[146:149], v[216:219], v[100:103]
	v_mfma_f32_16x16x32_bf16 v[96:99], v[166:169], v[216:219], v[96:99]
	v_mfma_f32_16x16x32_bf16 v[84:87], v[146:149], v[224:227], v[84:87]
	v_mfma_f32_16x16x32_bf16 v[80:83], v[166:169], v[224:227], v[80:83]
	v_mfma_f32_16x16x32_bf16 v[68:71], v[146:149], v[232:235], v[68:71]
	v_mfma_f32_16x16x32_bf16 v[64:67], v[166:169], v[232:235], v[64:67]
	v_mfma_f32_16x16x32_bf16 v[112:115], v[150:153], v[202:205], v[112:115]
	v_mfma_f32_16x16x32_bf16 v[104:107], v[170:173], v[202:205], v[104:107]
	v_mfma_f32_16x16x32_bf16 v[100:103], v[150:153], v[220:223], v[100:103]
	v_mfma_f32_16x16x32_bf16 v[96:99], v[170:173], v[220:223], v[96:99]
	v_mfma_f32_16x16x32_bf16 v[84:87], v[150:153], v[228:231], v[84:87]
	v_mfma_f32_16x16x32_bf16 v[80:83], v[170:173], v[228:231], v[80:83]
	v_mfma_f32_16x16x32_bf16 v[68:71], v[150:153], v[236:239], v[68:71]
	v_mfma_f32_16x16x32_bf16 v[64:67], v[170:173], v[236:239], v[64:67]
	s_setprio 0
	s_barrier
	s_add_i32 s66, s66, s0
	v_lshl_add_u64 v[206:207], s[56:57], 0, v[128:129]
	s_mov_b32 m0, s66
	ds_read_b128 v[174:177], v197 offset:16384
	ds_read_b128 v[202:205], v197 offset:17408
	ds_read_b128 v[216:219], v197 offset:18432
	ds_read_b128 v[220:223], v197 offset:19456
	ds_read_b128 v[224:227], v197 offset:20480
	ds_read_b128 v[228:231], v197 offset:21504
	ds_read_b128 v[232:235], v197 offset:22528
	ds_read_b128 v[236:239], v197 offset:23552
	global_load_lds_dwordx4 v[206:207], off
	s_add_i32 m0, s66, 0x2000
	s_add_u32 s66, s56, 0x40000
	v_lshl_add_u64 v[240:241], s[56:57], 0, v[158:159]
	s_addc_u32 s67, s57, 0
	s_add_i32 s68, s68, s0
	global_load_lds_dwordx4 v[240:241], off
	v_lshl_add_u64 v[242:243], s[66:67], 0, v[128:129]
	s_mov_b32 m0, s68
	v_lshl_add_u64 v[244:245], s[58:59], 0, v[156:157]
	global_load_lds_dwordx4 v[242:243], off
	v_lshl_add_u64 v[242:243], s[66:67], 0, v[158:159]
	s_add_i32 m0, s68, 0x2000
	s_nop 0
	global_load_lds_dwordx4 v[242:243], off
	v_lshl_add_u64 v[242:243], s[58:59], 0, v[154:155]
	s_mov_b32 m0, s1
	s_nop 0
	global_load_lds_dwordx4 v[242:243], off
	s_mov_b32 m0, s33
	s_nop 0
	global_load_lds_dwordx4 v[244:245], off
	s_waitcnt vmcnt(24)
	s_waitcnt lgkmcnt(0)
	s_barrier
	s_setprio 1
	s_waitcnt lgkmcnt(0)
	v_mfma_f32_16x16x32_bf16 v[60:63], v[130:133], v[174:177], v[60:63]
	v_mfma_f32_16x16x32_bf16 v[56:59], v[138:141], v[174:177], v[56:59]
	v_mfma_f32_16x16x32_bf16 v[44:47], v[130:133], v[216:219], v[44:47]
	v_mfma_f32_16x16x32_bf16 v[40:43], v[138:141], v[216:219], v[40:43]
	v_mfma_f32_16x16x32_bf16 v[28:31], v[130:133], v[224:227], v[28:31]
	v_mfma_f32_16x16x32_bf16 v[24:27], v[138:141], v[224:227], v[24:27]
	v_mfma_f32_16x16x32_bf16 v[12:15], v[130:133], v[232:235], v[12:15]
	v_mfma_f32_16x16x32_bf16 v[8:11], v[138:141], v[232:235], v[8:11]
	v_mfma_f32_16x16x32_bf16 v[60:63], v[134:137], v[202:205], v[60:63]
	v_mfma_f32_16x16x32_bf16 v[56:59], v[142:145], v[202:205], v[56:59]
	v_mfma_f32_16x16x32_bf16 v[44:47], v[134:137], v[220:223], v[44:47]
	v_mfma_f32_16x16x32_bf16 v[40:43], v[142:145], v[220:223], v[40:43]
	v_mfma_f32_16x16x32_bf16 v[28:31], v[134:137], v[228:231], v[28:31]
	v_mfma_f32_16x16x32_bf16 v[24:27], v[142:145], v[228:231], v[24:27]
	v_mfma_f32_16x16x32_bf16 v[12:15], v[134:137], v[236:239], v[12:15]
	v_mfma_f32_16x16x32_bf16 v[8:11], v[142:145], v[236:239], v[8:11]
	s_setprio 0
	s_setprio 1
	v_mfma_f32_16x16x32_bf16 v[52:55], v[146:149], v[174:177], v[52:55]
	v_mfma_f32_16x16x32_bf16 v[48:51], v[166:169], v[174:177], v[48:51]
	v_mfma_f32_16x16x32_bf16 v[36:39], v[146:149], v[216:219], v[36:39]
	v_mfma_f32_16x16x32_bf16 v[32:35], v[166:169], v[216:219], v[32:35]
	v_mfma_f32_16x16x32_bf16 v[20:23], v[146:149], v[224:227], v[20:23]
	v_mfma_f32_16x16x32_bf16 v[16:19], v[166:169], v[224:227], v[16:19]
	v_mfma_f32_16x16x32_bf16 v[4:7], v[146:149], v[232:235], v[4:7]
	v_mfma_f32_16x16x32_bf16 v[0:3], v[166:169], v[232:235], v[0:3]
	v_mfma_f32_16x16x32_bf16 v[52:55], v[150:153], v[202:205], v[52:55]
	v_mfma_f32_16x16x32_bf16 v[48:51], v[170:173], v[202:205], v[48:51]
	v_mfma_f32_16x16x32_bf16 v[36:39], v[150:153], v[220:223], v[36:39]
	v_mfma_f32_16x16x32_bf16 v[32:35], v[170:173], v[220:223], v[32:35]
	v_mfma_f32_16x16x32_bf16 v[20:23], v[150:153], v[228:231], v[20:23]
	v_mfma_f32_16x16x32_bf16 v[16:19], v[170:173], v[228:231], v[16:19]
	v_mfma_f32_16x16x32_bf16 v[4:7], v[150:153], v[236:239], v[4:7]
	v_mfma_f32_16x16x32_bf16 v[0:3], v[170:173], v[236:239], v[0:3]
	s_setprio 0
	s_barrier
	s_branch .Lp6_mid

.Lp6_mid:
	s_add_i32 s66, 0, 0x18000
	s_add_i32 s67, 0, 0x1c000
	v_add_u32_e32 v142, s66, v190
	v_add_u32_e32 v170, s67, v190
	ds_read_b128 v[130:133], v142
	ds_read_b128 v[134:137], v142 offset:1024
	ds_read_b128 v[138:141], v142 offset:2048
	ds_read_b128 v[142:145], v142 offset:3072
	ds_read_b128 v[146:149], v170
	ds_read_b128 v[150:153], v170 offset:1024
	ds_read_b128 v[166:169], v170 offset:2048
	ds_read_b128 v[170:173], v170 offset:3072
	s_add_u32 s58, s58, 0x40000
	s_addc_u32 s59, s59, 0
	s_mov_b32 m0, s60
	v_lshl_add_u64 v[246:247], s[58:59], 0, v[154:155]
	ds_read_b128 v[174:177], v197 offset:32768
	ds_read_b128 v[202:205], v197 offset:33792
	ds_read_b128 v[216:219], v197 offset:34816
	ds_read_b128 v[220:223], v197 offset:35840
	ds_read_b128 v[224:227], v197 offset:36864
	ds_read_b128 v[228:231], v197 offset:37888
	ds_read_b128 v[232:235], v197 offset:38912
	ds_read_b128 v[236:239], v197 offset:39936
	global_load_lds_dwordx4 v[246:247], off
	v_lshl_add_u64 v[246:247], s[58:59], 0, v[156:157]
	s_mov_b32 m0, s61
	s_nop 0
	global_load_lds_dwordx4 v[246:247], off
	s_waitcnt vmcnt(8)
	s_waitcnt lgkmcnt(0)
	s_barrier
	s_setprio 1
	s_waitcnt lgkmcnt(0)
	v_mfma_f32_16x16x32_bf16 v[124:127], v[130:133], v[174:177], v[124:127]
	v_mfma_f32_16x16x32_bf16 v[120:123], v[138:141], v[174:177], v[120:123]
	v_mfma_f32_16x16x32_bf16 v[116:119], v[130:133], v[216:219], v[116:119]
	v_mfma_f32_16x16x32_bf16 v[108:111], v[138:141], v[216:219], v[108:111]
	v_mfma_f32_16x16x32_bf16 v[92:95], v[130:133], v[224:227], v[92:95]
	v_mfma_f32_16x16x32_bf16 v[88:91], v[138:141], v[224:227], v[88:91]
	v_mfma_f32_16x16x32_bf16 v[76:79], v[130:133], v[232:235], v[76:79]
	v_mfma_f32_16x16x32_bf16 v[72:75], v[138:141], v[232:235], v[72:75]
	v_mfma_f32_16x16x32_bf16 v[124:127], v[134:137], v[202:205], v[124:127]
	v_mfma_f32_16x16x32_bf16 v[120:123], v[142:145], v[202:205], v[120:123]
	v_mfma_f32_16x16x32_bf16 v[116:119], v[134:137], v[220:223], v[116:119]
	v_mfma_f32_16x16x32_bf16 v[108:111], v[142:145], v[220:223], v[108:111]
	v_mfma_f32_16x16x32_bf16 v[92:95], v[134:137], v[228:231], v[92:95]
	v_mfma_f32_16x16x32_bf16 v[88:91], v[142:145], v[228:231], v[88:91]
	v_mfma_f32_16x16x32_bf16 v[76:79], v[134:137], v[236:239], v[76:79]
	v_mfma_f32_16x16x32_bf16 v[72:75], v[142:145], v[236:239], v[72:75]
	s_setprio 0
	s_setprio 1
	v_mfma_f32_16x16x32_bf16 v[112:115], v[146:149], v[174:177], v[112:115]
	v_mfma_f32_16x16x32_bf16 v[104:107], v[166:169], v[174:177], v[104:107]
	v_mfma_f32_16x16x32_bf16 v[100:103], v[146:149], v[216:219], v[100:103]
	v_mfma_f32_16x16x32_bf16 v[96:99], v[166:169], v[216:219], v[96:99]
	v_mfma_f32_16x16x32_bf16 v[84:87], v[146:149], v[224:227], v[84:87]
	v_mfma_f32_16x16x32_bf16 v[80:83], v[166:169], v[224:227], v[80:83]
	v_mfma_f32_16x16x32_bf16 v[68:71], v[146:149], v[232:235], v[68:71]
	v_mfma_f32_16x16x32_bf16 v[64:67], v[166:169], v[232:235], v[64:67]
	v_mfma_f32_16x16x32_bf16 v[112:115], v[150:153], v[202:205], v[112:115]
	v_mfma_f32_16x16x32_bf16 v[104:107], v[170:173], v[202:205], v[104:107]
	v_mfma_f32_16x16x32_bf16 v[100:103], v[150:153], v[220:223], v[100:103]
	v_mfma_f32_16x16x32_bf16 v[96:99], v[170:173], v[220:223], v[96:99]
	v_mfma_f32_16x16x32_bf16 v[84:87], v[150:153], v[228:231], v[84:87]
	v_mfma_f32_16x16x32_bf16 v[80:83], v[170:173], v[228:231], v[80:83]
	v_mfma_f32_16x16x32_bf16 v[68:71], v[150:153], v[236:239], v[68:71]
	v_mfma_f32_16x16x32_bf16 v[64:67], v[170:173], v[236:239], v[64:67]
	s_setprio 0
	s_barrier
	s_add_i32 s58, s66, s0
	v_lshl_add_u64 v[206:207], v[206:207], 0, s[88:89]
	s_mov_b32 m0, s58
	ds_read_b128 v[174:177], v197 offset:49152
	ds_read_b128 v[202:205], v197 offset:50176
	ds_read_b128 v[216:219], v197 offset:51200
	ds_read_b128 v[220:223], v197 offset:52224
	ds_read_b128 v[224:227], v197 offset:53248
	ds_read_b128 v[228:231], v197 offset:54272
	ds_read_b128 v[232:235], v197 offset:55296
	ds_read_b128 v[236:239], v197 offset:56320
	global_load_lds_dwordx4 v[206:207], off
	s_add_i32 m0, s58, 0x2000
	s_add_u32 s56, s56, 0x40080
	v_lshl_add_u64 v[206:207], v[240:241], 0, s[88:89]
	s_addc_u32 s57, s57, 0
	s_add_i32 s58, s67, s0
	global_load_lds_dwordx4 v[206:207], off
	v_lshl_add_u64 v[206:207], s[56:57], 0, v[128:129]
	s_mov_b32 m0, s58
	s_nop 0
	global_load_lds_dwordx4 v[206:207], off
	v_lshl_add_u64 v[206:207], s[56:57], 0, v[158:159]
	s_add_i32 m0, s58, 0x2000
	s_nop 0
	global_load_lds_dwordx4 v[206:207], off
	v_lshl_add_u64 v[206:207], v[242:243], 0, s[88:89]
	s_mov_b32 m0, s62
	s_nop 0
	global_load_lds_dwordx4 v[206:207], off
	v_lshl_add_u64 v[206:207], v[244:245], 0, s[88:89]
	s_mov_b32 m0, s63
	s_nop 0
	global_load_lds_dwordx4 v[206:207], off
	s_waitcnt vmcnt(8)
	s_waitcnt lgkmcnt(0)
	s_barrier
	s_setprio 1
	s_waitcnt lgkmcnt(0)
	v_mfma_f32_16x16x32_bf16 v[60:63], v[130:133], v[174:177], v[60:63]
	v_mfma_f32_16x16x32_bf16 v[56:59], v[138:141], v[174:177], v[56:59]
	v_mfma_f32_16x16x32_bf16 v[44:47], v[130:133], v[216:219], v[44:47]
	v_mfma_f32_16x16x32_bf16 v[40:43], v[138:141], v[216:219], v[40:43]
	v_mfma_f32_16x16x32_bf16 v[28:31], v[130:133], v[224:227], v[28:31]
	v_mfma_f32_16x16x32_bf16 v[24:27], v[138:141], v[224:227], v[24:27]
	v_mfma_f32_16x16x32_bf16 v[12:15], v[130:133], v[232:235], v[12:15]
	v_mfma_f32_16x16x32_bf16 v[8:11], v[138:141], v[232:235], v[8:11]
	v_mfma_f32_16x16x32_bf16 v[60:63], v[134:137], v[202:205], v[60:63]
	v_mfma_f32_16x16x32_bf16 v[56:59], v[142:145], v[202:205], v[56:59]
	v_mfma_f32_16x16x32_bf16 v[44:47], v[134:137], v[220:223], v[44:47]
	v_mfma_f32_16x16x32_bf16 v[40:43], v[142:145], v[220:223], v[40:43]
	v_mfma_f32_16x16x32_bf16 v[28:31], v[134:137], v[228:231], v[28:31]
	v_mfma_f32_16x16x32_bf16 v[24:27], v[142:145], v[228:231], v[24:27]
	v_mfma_f32_16x16x32_bf16 v[12:15], v[134:137], v[236:239], v[12:15]
	v_mfma_f32_16x16x32_bf16 v[8:11], v[142:145], v[236:239], v[8:11]
	s_setprio 0
	s_setprio 1
	v_mfma_f32_16x16x32_bf16 v[52:55], v[146:149], v[174:177], v[52:55]
	v_mfma_f32_16x16x32_bf16 v[48:51], v[166:169], v[174:177], v[48:51]
	v_mfma_f32_16x16x32_bf16 v[36:39], v[146:149], v[216:219], v[36:39]
	v_mfma_f32_16x16x32_bf16 v[32:35], v[166:169], v[216:219], v[32:35]
	v_mfma_f32_16x16x32_bf16 v[20:23], v[146:149], v[224:227], v[20:23]
	v_mfma_f32_16x16x32_bf16 v[16:19], v[166:169], v[224:227], v[16:19]
	v_mfma_f32_16x16x32_bf16 v[4:7], v[146:149], v[232:235], v[4:7]
	v_mfma_f32_16x16x32_bf16 v[0:3], v[166:169], v[232:235], v[0:3]
	v_mfma_f32_16x16x32_bf16 v[52:55], v[150:153], v[202:205], v[52:55]
	v_mfma_f32_16x16x32_bf16 v[48:51], v[170:173], v[202:205], v[48:51]
	v_mfma_f32_16x16x32_bf16 v[36:39], v[150:153], v[220:223], v[36:39]
	v_mfma_f32_16x16x32_bf16 v[32:35], v[170:173], v[220:223], v[32:35]
	v_mfma_f32_16x16x32_bf16 v[20:23], v[150:153], v[228:231], v[20:23]
	v_mfma_f32_16x16x32_bf16 v[16:19], v[170:173], v[228:231], v[16:19]
	v_mfma_f32_16x16x32_bf16 v[4:7], v[150:153], v[236:239], v[4:7]
	v_mfma_f32_16x16x32_bf16 v[0:3], v[170:173], v[236:239], v[0:3]
	s_setprio 0
	s_barrier
	s_add_i32 s49, s49, 2
	s_add_u32 s54, s54, 0x100
	s_addc_u32 s55, s55, 0
	s_add_u32 s27, s27, 0x100
	s_addc_u32 s47, s47, 0
	s_cmp_gt_u32 s49, 13
	s_cbranch_scc0 .LBB0_1278
	s_and_b64 vcc, exec, s[44:45]
	s_cbranch_vccz .LBB0_1281
	s_barrier

.LBB0_1439:
	s_or_b64 exec, exec, s[62:63]
	s_add_u32 s58, s58, 0x40080
	s_addc_u32 s59, s59, 0
	s_add_u32 s9, s60, 0x100
	v_mov_b32_e32 v0, 0
	s_addc_u32 s27, s61, 0
	s_mov_b32 s31, -2
	v_mov_b32_e32 v1, v0
	v_mov_b32_e32 v2, v0
	v_mov_b32_e32 v3, v0
	v_mov_b32_e32 v4, v0
	v_mov_b32_e32 v5, v0
	v_mov_b32_e32 v6, v0
	v_mov_b32_e32 v7, v0
	v_mov_b32_e32 v16, v0
	v_mov_b32_e32 v17, v0
	v_mov_b32_e32 v18, v0
	v_mov_b32_e32 v19, v0
	v_mov_b32_e32 v20, v0
	v_mov_b32_e32 v21, v0
	v_mov_b32_e32 v22, v0
	v_mov_b32_e32 v23, v0
	v_mov_b32_e32 v32, v0
	v_mov_b32_e32 v33, v0
	v_mov_b32_e32 v34, v0
	v_mov_b32_e32 v35, v0
	v_mov_b32_e32 v36, v0
	v_mov_b32_e32 v37, v0
	v_mov_b32_e32 v38, v0
	v_mov_b32_e32 v39, v0
	v_mov_b32_e32 v48, v0
	v_mov_b32_e32 v49, v0
	v_mov_b32_e32 v50, v0
	v_mov_b32_e32 v51, v0
	v_mov_b32_e32 v52, v0
	v_mov_b32_e32 v53, v0
	v_mov_b32_e32 v54, v0
	v_mov_b32_e32 v55, v0
	v_mov_b32_e32 v8, v0
	v_mov_b32_e32 v9, v0
	v_mov_b32_e32 v10, v0
	v_mov_b32_e32 v11, v0
	v_mov_b32_e32 v12, v0
	v_mov_b32_e32 v13, v0
	v_mov_b32_e32 v14, v0
	v_mov_b32_e32 v15, v0
	v_mov_b32_e32 v24, v0
	v_mov_b32_e32 v25, v0
	v_mov_b32_e32 v26, v0
	v_mov_b32_e32 v27, v0
	v_mov_b32_e32 v28, v0
	v_mov_b32_e32 v29, v0
	v_mov_b32_e32 v30, v0
	v_mov_b32_e32 v31, v0
	v_mov_b32_e32 v40, v0
	v_mov_b32_e32 v41, v0
	v_mov_b32_e32 v42, v0
	v_mov_b32_e32 v43, v0
	v_mov_b32_e32 v44, v0
	v_mov_b32_e32 v45, v0
	v_mov_b32_e32 v46, v0
	v_mov_b32_e32 v47, v0
	v_mov_b32_e32 v56, v0
	v_mov_b32_e32 v57, v0
	v_mov_b32_e32 v58, v0
	v_mov_b32_e32 v59, v0
	v_mov_b32_e32 v60, v0
	v_mov_b32_e32 v61, v0
	v_mov_b32_e32 v62, v0
	v_mov_b32_e32 v63, v0
	v_mov_b32_e32 v64, v0
	v_mov_b32_e32 v65, v0
	v_mov_b32_e32 v66, v0
	v_mov_b32_e32 v67, v0
	v_mov_b32_e32 v68, v0
	v_mov_b32_e32 v69, v0
	v_mov_b32_e32 v70, v0
	v_mov_b32_e32 v71, v0
	v_mov_b32_e32 v80, v0
	v_mov_b32_e32 v81, v0
	v_mov_b32_e32 v82, v0
	v_mov_b32_e32 v83, v0
	v_mov_b32_e32 v84, v0
	v_mov_b32_e32 v85, v0
	v_mov_b32_e32 v86, v0
	v_mov_b32_e32 v87, v0
	v_mov_b32_e32 v96, v0
	v_mov_b32_e32 v97, v0
	v_mov_b32_e32 v98, v0
	v_mov_b32_e32 v99, v0
	v_mov_b32_e32 v100, v0
	v_mov_b32_e32 v101, v0
	v_mov_b32_e32 v102, v0
	v_mov_b32_e32 v103, v0
	v_mov_b32_e32 v112, v0
	v_mov_b32_e32 v113, v0
	v_mov_b32_e32 v114, v0
	v_mov_b32_e32 v115, v0
	v_mov_b32_e32 v116, v0
	v_mov_b32_e32 v117, v0
	v_mov_b32_e32 v118, v0
	v_mov_b32_e32 v119, v0
	v_mov_b32_e32 v72, v0
	v_mov_b32_e32 v73, v0
	v_mov_b32_e32 v74, v0
	v_mov_b32_e32 v75, v0
	v_mov_b32_e32 v76, v0
	v_mov_b32_e32 v77, v0
	v_mov_b32_e32 v78, v0
	v_mov_b32_e32 v79, v0
	v_mov_b32_e32 v88, v0
	v_mov_b32_e32 v89, v0
	v_mov_b32_e32 v90, v0
	v_mov_b32_e32 v91, v0
	v_mov_b32_e32 v92, v0
	v_mov_b32_e32 v93, v0
	v_mov_b32_e32 v94, v0
	v_mov_b32_e32 v95, v0
	v_mov_b32_e32 v104, v0
	v_mov_b32_e32 v105, v0
	v_mov_b32_e32 v106, v0
	v_mov_b32_e32 v107, v0
	v_mov_b32_e32 v108, v0
	v_mov_b32_e32 v109, v0
	v_mov_b32_e32 v110, v0
	v_mov_b32_e32 v111, v0
	v_mov_b32_e32 v120, v0
	v_mov_b32_e32 v121, v0
	v_mov_b32_e32 v122, v0
	v_mov_b32_e32 v123, v0
	v_mov_b32_e32 v124, v0
	v_mov_b32_e32 v125, v0
	v_mov_b32_e32 v126, v0
	v_mov_b32_e32 v127, v0
	s_cmp_eq_u32 s8, 0
	s_cbranch_scc1 .LBB0_1440
	s_add_u32 s47, s58, 0xfffc0080
	s_addc_u32 s53, s59, -1
	s_add_i32 s55, 0, 0x10000
	s_cmp_eq_u32 s31, 12
	s_cselect_b32 s63, s49, s53
	s_cselect_b32 s62, s48, s47
	v_add_u32_e32 v150, s55, v153
	s_cselect_b32 s61, s51, s27
	s_cselect_b32 s60, s50, s9
	s_add_i32 s47, 0, 0x14000
	ds_read_b128 v[142:145], v150
	ds_read_b128 v[146:149], v150 offset:1024
	ds_read_b128 v[182:185], v150 offset:2048
	ds_read_b128 v[186:189], v150 offset:3072
	v_add_u32_e32 v150, s47, v153
	ds_read_b128 v[190:193], v150
	ds_read_b128 v[194:197], v150 offset:1024
	ds_read_b128 v[200:203], v150 offset:2048
	ds_read_b128 v[216:219], v150 offset:3072
	v_lshl_add_u64 v[150:151], s[58:59], 0, v[138:139]
	s_add_i32 m0, s1, 0xc000
	ds_read_b128 v[220:223], v165
	ds_read_b128 v[224:227], v165 offset:1024
	ds_read_b128 v[228:231], v165 offset:2048
	ds_read_b128 v[232:235], v165 offset:3072
	ds_read_b128 v[236:239], v165 offset:4096
	ds_read_b128 v[240:243], v165 offset:5120
	ds_read_b128 v[244:247], v165 offset:6144
	ds_read_b128 v[204:207], v165 offset:7168
	global_load_lds_dwordx4 v[150:151], off
	v_lshl_add_u64 v[150:151], s[58:59], 0, v[140:141]
	s_add_i32 m0, s1, 0xe000
	s_nop 0
	global_load_lds_dwordx4 v[150:151], off
	s_waitcnt vmcnt(24)
	s_waitcnt lgkmcnt(0)
	s_barrier
	s_setprio 1
	s_waitcnt lgkmcnt(0)
	v_mfma_f32_16x16x32_bf16 v[124:127], v[142:145], v[220:223], v[124:127]
	v_mfma_f32_16x16x32_bf16 v[120:123], v[182:185], v[220:223], v[120:123]
	v_mfma_f32_16x16x32_bf16 v[108:111], v[142:145], v[228:231], v[108:111]
	v_mfma_f32_16x16x32_bf16 v[104:107], v[182:185], v[228:231], v[104:107]
	v_mfma_f32_16x16x32_bf16 v[92:95], v[142:145], v[236:239], v[92:95]
	v_mfma_f32_16x16x32_bf16 v[88:91], v[182:185], v[236:239], v[88:91]
	v_mfma_f32_16x16x32_bf16 v[76:79], v[142:145], v[244:247], v[76:79]
	v_mfma_f32_16x16x32_bf16 v[72:75], v[182:185], v[244:247], v[72:75]
	v_mfma_f32_16x16x32_bf16 v[124:127], v[146:149], v[224:227], v[124:127]
	v_mfma_f32_16x16x32_bf16 v[120:123], v[186:189], v[224:227], v[120:123]
	v_mfma_f32_16x16x32_bf16 v[108:111], v[146:149], v[232:235], v[108:111]
	v_mfma_f32_16x16x32_bf16 v[104:107], v[186:189], v[232:235], v[104:107]
	v_mfma_f32_16x16x32_bf16 v[92:95], v[146:149], v[240:243], v[92:95]
	v_mfma_f32_16x16x32_bf16 v[88:91], v[186:189], v[240:243], v[88:91]
	v_mfma_f32_16x16x32_bf16 v[76:79], v[146:149], v[204:207], v[76:79]
	v_mfma_f32_16x16x32_bf16 v[72:75], v[186:189], v[204:207], v[72:75]
	s_setprio 0
	s_setprio 1
	v_mfma_f32_16x16x32_bf16 v[116:119], v[190:193], v[220:223], v[116:119]
	v_mfma_f32_16x16x32_bf16 v[112:115], v[200:203], v[220:223], v[112:115]
	v_mfma_f32_16x16x32_bf16 v[100:103], v[190:193], v[228:231], v[100:103]
	v_mfma_f32_16x16x32_bf16 v[96:99], v[200:203], v[228:231], v[96:99]
	v_mfma_f32_16x16x32_bf16 v[84:87], v[190:193], v[236:239], v[84:87]
	v_mfma_f32_16x16x32_bf16 v[80:83], v[200:203], v[236:239], v[80:83]
	v_mfma_f32_16x16x32_bf16 v[68:71], v[190:193], v[244:247], v[68:71]
	v_mfma_f32_16x16x32_bf16 v[64:67], v[200:203], v[244:247], v[64:67]
	v_mfma_f32_16x16x32_bf16 v[116:119], v[194:197], v[224:227], v[116:119]
	v_mfma_f32_16x16x32_bf16 v[112:115], v[216:219], v[224:227], v[112:115]
	v_mfma_f32_16x16x32_bf16 v[100:103], v[194:197], v[232:235], v[100:103]
	v_mfma_f32_16x16x32_bf16 v[96:99], v[216:219], v[232:235], v[96:99]
	v_mfma_f32_16x16x32_bf16 v[84:87], v[194:197], v[240:243], v[84:87]
	v_mfma_f32_16x16x32_bf16 v[80:83], v[216:219], v[240:243], v[80:83]
	v_mfma_f32_16x16x32_bf16 v[68:71], v[194:197], v[204:207], v[68:71]
	v_mfma_f32_16x16x32_bf16 v[64:67], v[216:219], v[204:207], v[64:67]
	s_setprio 0
	s_barrier
	s_add_i32 s53, s55, s0
	v_lshl_add_u64 v[150:151], s[60:61], 0, v[128:129]
	s_mov_b32 m0, s53
	ds_read_b128 v[204:207], v165 offset:16384
	ds_read_b128 v[220:223], v165 offset:17408
	ds_read_b128 v[224:227], v165 offset:18432
	ds_read_b128 v[228:231], v165 offset:19456
	ds_read_b128 v[232:235], v165 offset:20480
	ds_read_b128 v[236:239], v165 offset:21504
	ds_read_b128 v[240:243], v165 offset:22528
	ds_read_b128 v[244:247], v165 offset:23552
	global_load_lds_dwordx4 v[150:151], off
	s_add_i32 m0, s53, 0x2000
	s_add_u32 s70, s60, 0x40000
	v_lshl_add_u64 v[208:209], s[60:61], 0, v[134:135]
	s_addc_u32 s71, s61, 0
	s_add_i32 s47, s47, s0
	global_load_lds_dwordx4 v[208:209], off
	v_lshl_add_u64 v[248:249], s[70:71], 0, v[128:129]
	s_mov_b32 m0, s47
	v_lshl_add_u64 v[210:211], s[62:63], 0, v[132:133]
	global_load_lds_dwordx4 v[248:249], off
	v_lshl_add_u64 v[248:249], s[70:71], 0, v[134:135]
	s_add_i32 m0, s47, 0x2000
	s_nop 0
	global_load_lds_dwordx4 v[248:249], off
	v_lshl_add_u64 v[248:249], s[62:63], 0, v[130:131]
	s_mov_b32 m0, s1
	s_nop 0
	global_load_lds_dwordx4 v[248:249], off
	s_mov_b32 m0, s57
	s_nop 0
	global_load_lds_dwordx4 v[210:211], off
	s_waitcnt vmcnt(24)
	s_waitcnt lgkmcnt(0)
	s_barrier
	s_setprio 1
	s_waitcnt lgkmcnt(0)
	v_mfma_f32_16x16x32_bf16 v[60:63], v[142:145], v[204:207], v[60:63]
	v_mfma_f32_16x16x32_bf16 v[56:59], v[182:185], v[204:207], v[56:59]
	v_mfma_f32_16x16x32_bf16 v[44:47], v[142:145], v[224:227], v[44:47]
	v_mfma_f32_16x16x32_bf16 v[40:43], v[182:185], v[224:227], v[40:43]
	v_mfma_f32_16x16x32_bf16 v[28:31], v[142:145], v[232:235], v[28:31]
	v_mfma_f32_16x16x32_bf16 v[24:27], v[182:185], v[232:235], v[24:27]
	v_mfma_f32_16x16x32_bf16 v[12:15], v[142:145], v[240:243], v[12:15]
	v_mfma_f32_16x16x32_bf16 v[8:11], v[182:185], v[240:243], v[8:11]
	v_mfma_f32_16x16x32_bf16 v[60:63], v[146:149], v[220:223], v[60:63]
	v_mfma_f32_16x16x32_bf16 v[56:59], v[186:189], v[220:223], v[56:59]
	v_mfma_f32_16x16x32_bf16 v[44:47], v[146:149], v[228:231], v[44:47]
	v_mfma_f32_16x16x32_bf16 v[40:43], v[186:189], v[228:231], v[40:43]
	v_mfma_f32_16x16x32_bf16 v[28:31], v[146:149], v[236:239], v[28:31]
	v_mfma_f32_16x16x32_bf16 v[24:27], v[186:189], v[236:239], v[24:27]
	v_mfma_f32_16x16x32_bf16 v[12:15], v[146:149], v[244:247], v[12:15]
	v_mfma_f32_16x16x32_bf16 v[8:11], v[186:189], v[244:247], v[8:11]
	s_setprio 0
	s_setprio 1
	v_mfma_f32_16x16x32_bf16 v[52:55], v[190:193], v[204:207], v[52:55]
	v_mfma_f32_16x16x32_bf16 v[48:51], v[200:203], v[204:207], v[48:51]
	v_mfma_f32_16x16x32_bf16 v[36:39], v[190:193], v[224:227], v[36:39]
	v_mfma_f32_16x16x32_bf16 v[32:35], v[200:203], v[224:227], v[32:35]
	v_mfma_f32_16x16x32_bf16 v[20:23], v[190:193], v[232:235], v[20:23]
	v_mfma_f32_16x16x32_bf16 v[16:19], v[200:203], v[232:235], v[16:19]
	v_mfma_f32_16x16x32_bf16 v[4:7], v[190:193], v[240:243], v[4:7]
	v_mfma_f32_16x16x32_bf16 v[0:3], v[200:203], v[240:243], v[0:3]
	v_mfma_f32_16x16x32_bf16 v[52:55], v[194:197], v[220:223], v[52:55]
	v_mfma_f32_16x16x32_bf16 v[48:51], v[216:219], v[220:223], v[48:51]
	v_mfma_f32_16x16x32_bf16 v[36:39], v[194:197], v[228:231], v[36:39]
	v_mfma_f32_16x16x32_bf16 v[32:35], v[216:219], v[228:231], v[32:35]
	v_mfma_f32_16x16x32_bf16 v[20:23], v[194:197], v[236:239], v[20:23]
	v_mfma_f32_16x16x32_bf16 v[16:19], v[216:219], v[236:239], v[16:19]
	v_mfma_f32_16x16x32_bf16 v[4:7], v[194:197], v[244:247], v[4:7]
	v_mfma_f32_16x16x32_bf16 v[0:3], v[216:219], v[244:247], v[0:3]
	s_setprio 0
	s_barrier
	s_branch .Lp8_mid

.Lp8_mid:
	s_add_i32 s47, 0, 0x18000
	v_add_u32_e32 v181, s47, v153
	s_add_i32 s53, 0, 0x1c000
	ds_read_b128 v[142:145], v181
	ds_read_b128 v[146:149], v181 offset:1024
	ds_read_b128 v[182:185], v181 offset:2048
	ds_read_b128 v[186:189], v181 offset:3072
	v_add_u32_e32 v181, s53, v153
	ds_read_b128 v[190:193], v181
	ds_read_b128 v[194:197], v181 offset:1024
	ds_read_b128 v[200:203], v181 offset:2048
	ds_read_b128 v[204:207], v181 offset:3072
	s_add_u32 s62, s62, 0x40000
	s_addc_u32 s63, s63, 0
	s_mov_b32 m0, s64
	v_lshl_add_u64 v[214:215], s[62:63], 0, v[130:131]
	ds_read_b128 v[216:219], v165 offset:32768
	ds_read_b128 v[220:223], v165 offset:33792
	ds_read_b128 v[224:227], v165 offset:34816
	ds_read_b128 v[228:231], v165 offset:35840
	ds_read_b128 v[232:235], v165 offset:36864
	ds_read_b128 v[236:239], v165 offset:37888
	ds_read_b128 v[240:243], v165 offset:38912
	ds_read_b128 v[244:247], v165 offset:39936
	global_load_lds_dwordx4 v[214:215], off
	v_lshl_add_u64 v[214:215], s[62:63], 0, v[132:133]
	s_mov_b32 m0, s65
	s_nop 0
	global_load_lds_dwordx4 v[214:215], off
	s_waitcnt vmcnt(8)
	s_waitcnt lgkmcnt(0)
	s_barrier
	s_setprio 1
	s_waitcnt lgkmcnt(0)
	v_mfma_f32_16x16x32_bf16 v[124:127], v[142:145], v[216:219], v[124:127]
	v_mfma_f32_16x16x32_bf16 v[120:123], v[182:185], v[216:219], v[120:123]
	v_mfma_f32_16x16x32_bf16 v[108:111], v[142:145], v[224:227], v[108:111]
	v_mfma_f32_16x16x32_bf16 v[104:107], v[182:185], v[224:227], v[104:107]
	v_mfma_f32_16x16x32_bf16 v[92:95], v[142:145], v[232:235], v[92:95]
	v_mfma_f32_16x16x32_bf16 v[88:91], v[182:185], v[232:235], v[88:91]
	v_mfma_f32_16x16x32_bf16 v[76:79], v[142:145], v[240:243], v[76:79]
	v_mfma_f32_16x16x32_bf16 v[72:75], v[182:185], v[240:243], v[72:75]
	v_mfma_f32_16x16x32_bf16 v[124:127], v[146:149], v[220:223], v[124:127]
	v_mfma_f32_16x16x32_bf16 v[120:123], v[186:189], v[220:223], v[120:123]
	v_mfma_f32_16x16x32_bf16 v[108:111], v[146:149], v[228:231], v[108:111]
	v_mfma_f32_16x16x32_bf16 v[104:107], v[186:189], v[228:231], v[104:107]
	v_mfma_f32_16x16x32_bf16 v[92:95], v[146:149], v[236:239], v[92:95]
	v_mfma_f32_16x16x32_bf16 v[88:91], v[186:189], v[236:239], v[88:91]
	v_mfma_f32_16x16x32_bf16 v[76:79], v[146:149], v[244:247], v[76:79]
	v_mfma_f32_16x16x32_bf16 v[72:75], v[186:189], v[244:247], v[72:75]
	s_setprio 0
	s_setprio 1
	v_mfma_f32_16x16x32_bf16 v[116:119], v[190:193], v[216:219], v[116:119]
	v_mfma_f32_16x16x32_bf16 v[112:115], v[200:203], v[216:219], v[112:115]
	v_mfma_f32_16x16x32_bf16 v[100:103], v[190:193], v[224:227], v[100:103]
	v_mfma_f32_16x16x32_bf16 v[96:99], v[200:203], v[224:227], v[96:99]
	v_mfma_f32_16x16x32_bf16 v[84:87], v[190:193], v[232:235], v[84:87]
	v_mfma_f32_16x16x32_bf16 v[80:83], v[200:203], v[232:235], v[80:83]
	v_mfma_f32_16x16x32_bf16 v[68:71], v[190:193], v[240:243], v[68:71]
	v_mfma_f32_16x16x32_bf16 v[64:67], v[200:203], v[240:243], v[64:67]
	v_mfma_f32_16x16x32_bf16 v[116:119], v[194:197], v[220:223], v[116:119]
	v_mfma_f32_16x16x32_bf16 v[112:115], v[204:207], v[220:223], v[112:115]
	v_mfma_f32_16x16x32_bf16 v[100:103], v[194:197], v[228:231], v[100:103]
	v_mfma_f32_16x16x32_bf16 v[96:99], v[204:207], v[228:231], v[96:99]
	v_mfma_f32_16x16x32_bf16 v[84:87], v[194:197], v[236:239], v[84:87]
	v_mfma_f32_16x16x32_bf16 v[80:83], v[204:207], v[236:239], v[80:83]
	v_mfma_f32_16x16x32_bf16 v[68:71], v[194:197], v[244:247], v[68:71]
	v_mfma_f32_16x16x32_bf16 v[64:67], v[204:207], v[244:247], v[64:67]
	s_setprio 0
	s_barrier
	s_add_i32 s47, s47, s0
	v_lshl_add_u64 v[150:151], v[150:151], 0, s[88:89]
	s_mov_b32 m0, s47
	ds_read_b128 v[216:219], v165 offset:49152
	ds_read_b128 v[220:223], v165 offset:50176
	ds_read_b128 v[224:227], v165 offset:51200
	ds_read_b128 v[228:231], v165 offset:52224
	ds_read_b128 v[232:235], v165 offset:53248
	ds_read_b128 v[236:239], v165 offset:54272
	ds_read_b128 v[240:243], v165 offset:55296
	ds_read_b128 v[244:247], v165 offset:56320
	global_load_lds_dwordx4 v[150:151], off
	s_add_i32 m0, s47, 0x2000
	s_add_u32 s60, s60, 0x40080
	v_lshl_add_u64 v[150:151], v[208:209], 0, s[88:89]
	s_addc_u32 s61, s61, 0
	s_add_i32 s47, s53, s0
	global_load_lds_dwordx4 v[150:151], off
	v_lshl_add_u64 v[150:151], s[60:61], 0, v[128:129]
	s_mov_b32 m0, s47
	s_nop 0
	global_load_lds_dwordx4 v[150:151], off
	v_lshl_add_u64 v[150:151], s[60:61], 0, v[134:135]
	s_add_i32 m0, s47, 0x2000
	s_nop 0
	global_load_lds_dwordx4 v[150:151], off
	v_lshl_add_u64 v[150:151], v[248:249], 0, s[88:89]
	s_mov_b32 m0, s67
	s_nop 0
	global_load_lds_dwordx4 v[150:151], off
	v_lshl_add_u64 v[150:151], v[210:211], 0, s[88:89]
	s_mov_b32 m0, s68
	s_nop 0
	global_load_lds_dwordx4 v[150:151], off
	s_waitcnt vmcnt(8)
	s_waitcnt lgkmcnt(0)
	s_barrier
	s_setprio 1
	s_waitcnt lgkmcnt(0)
	v_mfma_f32_16x16x32_bf16 v[60:63], v[142:145], v[216:219], v[60:63]
	v_mfma_f32_16x16x32_bf16 v[56:59], v[182:185], v[216:219], v[56:59]
	v_mfma_f32_16x16x32_bf16 v[44:47], v[142:145], v[224:227], v[44:47]
	v_mfma_f32_16x16x32_bf16 v[40:43], v[182:185], v[224:227], v[40:43]
	v_mfma_f32_16x16x32_bf16 v[28:31], v[142:145], v[232:235], v[28:31]
	v_mfma_f32_16x16x32_bf16 v[24:27], v[182:185], v[232:235], v[24:27]
	v_mfma_f32_16x16x32_bf16 v[12:15], v[142:145], v[240:243], v[12:15]
	v_mfma_f32_16x16x32_bf16 v[8:11], v[182:185], v[240:243], v[8:11]
	v_mfma_f32_16x16x32_bf16 v[60:63], v[146:149], v[220:223], v[60:63]
	v_mfma_f32_16x16x32_bf16 v[56:59], v[186:189], v[220:223], v[56:59]
	v_mfma_f32_16x16x32_bf16 v[44:47], v[146:149], v[228:231], v[44:47]
	v_mfma_f32_16x16x32_bf16 v[40:43], v[186:189], v[228:231], v[40:43]
	v_mfma_f32_16x16x32_bf16 v[28:31], v[146:149], v[236:239], v[28:31]
	v_mfma_f32_16x16x32_bf16 v[24:27], v[186:189], v[236:239], v[24:27]
	v_mfma_f32_16x16x32_bf16 v[12:15], v[146:149], v[244:247], v[12:15]
	v_mfma_f32_16x16x32_bf16 v[8:11], v[186:189], v[244:247], v[8:11]
	s_setprio 0
	s_setprio 1
	v_mfma_f32_16x16x32_bf16 v[52:55], v[190:193], v[216:219], v[52:55]
	v_mfma_f32_16x16x32_bf16 v[48:51], v[200:203], v[216:219], v[48:51]
	v_mfma_f32_16x16x32_bf16 v[36:39], v[190:193], v[224:227], v[36:39]
	v_mfma_f32_16x16x32_bf16 v[32:35], v[200:203], v[224:227], v[32:35]
	v_mfma_f32_16x16x32_bf16 v[20:23], v[190:193], v[232:235], v[20:23]
	v_mfma_f32_16x16x32_bf16 v[16:19], v[200:203], v[232:235], v[16:19]
	v_mfma_f32_16x16x32_bf16 v[4:7], v[190:193], v[240:243], v[4:7]
	v_mfma_f32_16x16x32_bf16 v[0:3], v[200:203], v[240:243], v[0:3]
	v_mfma_f32_16x16x32_bf16 v[52:55], v[194:197], v[220:223], v[52:55]
	v_mfma_f32_16x16x32_bf16 v[48:51], v[204:207], v[220:223], v[48:51]
	v_mfma_f32_16x16x32_bf16 v[36:39], v[194:197], v[228:231], v[36:39]
	v_mfma_f32_16x16x32_bf16 v[32:35], v[204:207], v[228:231], v[32:35]
	v_mfma_f32_16x16x32_bf16 v[20:23], v[194:197], v[236:239], v[20:23]
	v_mfma_f32_16x16x32_bf16 v[16:19], v[204:207], v[236:239], v[16:19]
	v_mfma_f32_16x16x32_bf16 v[4:7], v[194:197], v[244:247], v[4:7]
	v_mfma_f32_16x16x32_bf16 v[0:3], v[204:207], v[244:247], v[0:3]
	s_setprio 0
	s_barrier
	s_add_i32 s31, s31, 2
	s_add_u32 s58, s58, 0x100
	s_addc_u32 s59, s59, 0
	s_add_u32 s9, s9, 0x100
	s_addc_u32 s27, s27, 0
	s_cmp_gt_u32 s31, 13
	s_cbranch_scc0 .LBB0_1440
	s_and_b64 vcc, exec, s[22:23]
	s_cbranch_vccz .LBB0_1443
	s_barrier

.LBB0_1583:
	s_add_u32 s58, s58, 0x40080
	s_addc_u32 s59, s59, 0
	s_add_u32 s8, s60, 0x100
	v_mov_b32_e32 v0, 0
	s_addc_u32 s9, s61, 0
	s_mov_b32 s23, -2
	v_mov_b32_e32 v1, v0
	v_mov_b32_e32 v2, v0
	v_mov_b32_e32 v3, v0
	v_mov_b32_e32 v4, v0
	v_mov_b32_e32 v5, v0
	v_mov_b32_e32 v6, v0
	v_mov_b32_e32 v7, v0
	v_mov_b32_e32 v16, v0
	v_mov_b32_e32 v17, v0
	v_mov_b32_e32 v18, v0
	v_mov_b32_e32 v19, v0
	v_mov_b32_e32 v20, v0
	v_mov_b32_e32 v21, v0
	v_mov_b32_e32 v22, v0
	v_mov_b32_e32 v23, v0
	v_mov_b32_e32 v32, v0
	v_mov_b32_e32 v33, v0
	v_mov_b32_e32 v34, v0
	v_mov_b32_e32 v35, v0
	v_mov_b32_e32 v36, v0
	v_mov_b32_e32 v37, v0
	v_mov_b32_e32 v38, v0
	v_mov_b32_e32 v39, v0
	v_mov_b32_e32 v48, v0
	v_mov_b32_e32 v49, v0
	v_mov_b32_e32 v50, v0
	v_mov_b32_e32 v51, v0
	v_mov_b32_e32 v52, v0
	v_mov_b32_e32 v53, v0
	v_mov_b32_e32 v54, v0
	v_mov_b32_e32 v55, v0
	v_mov_b32_e32 v8, v0
	v_mov_b32_e32 v9, v0
	v_mov_b32_e32 v10, v0
	v_mov_b32_e32 v11, v0
	v_mov_b32_e32 v12, v0
	v_mov_b32_e32 v13, v0
	v_mov_b32_e32 v14, v0
	v_mov_b32_e32 v15, v0
	v_mov_b32_e32 v24, v0
	v_mov_b32_e32 v25, v0
	v_mov_b32_e32 v26, v0
	v_mov_b32_e32 v27, v0
	v_mov_b32_e32 v28, v0
	v_mov_b32_e32 v29, v0
	v_mov_b32_e32 v30, v0
	v_mov_b32_e32 v31, v0
	v_mov_b32_e32 v40, v0
	v_mov_b32_e32 v41, v0
	v_mov_b32_e32 v42, v0
	v_mov_b32_e32 v43, v0
	v_mov_b32_e32 v44, v0
	v_mov_b32_e32 v45, v0
	v_mov_b32_e32 v46, v0
	v_mov_b32_e32 v47, v0
	v_mov_b32_e32 v56, v0
	v_mov_b32_e32 v57, v0
	v_mov_b32_e32 v58, v0
	v_mov_b32_e32 v59, v0
	v_mov_b32_e32 v60, v0
	v_mov_b32_e32 v61, v0
	v_mov_b32_e32 v62, v0
	v_mov_b32_e32 v63, v0
	v_mov_b32_e32 v64, v0
	v_mov_b32_e32 v65, v0
	v_mov_b32_e32 v66, v0
	v_mov_b32_e32 v67, v0
	v_mov_b32_e32 v68, v0
	v_mov_b32_e32 v69, v0
	v_mov_b32_e32 v70, v0
	v_mov_b32_e32 v71, v0
	v_mov_b32_e32 v80, v0
	v_mov_b32_e32 v81, v0
	v_mov_b32_e32 v82, v0
	v_mov_b32_e32 v83, v0
	v_mov_b32_e32 v84, v0
	v_mov_b32_e32 v85, v0
	v_mov_b32_e32 v86, v0
	v_mov_b32_e32 v87, v0
	v_mov_b32_e32 v96, v0
	v_mov_b32_e32 v97, v0
	v_mov_b32_e32 v98, v0
	v_mov_b32_e32 v99, v0
	v_mov_b32_e32 v100, v0
	v_mov_b32_e32 v101, v0
	v_mov_b32_e32 v102, v0
	v_mov_b32_e32 v103, v0
	v_mov_b32_e32 v104, v0
	v_mov_b32_e32 v105, v0
	v_mov_b32_e32 v106, v0
	v_mov_b32_e32 v107, v0
	v_mov_b32_e32 v112, v0
	v_mov_b32_e32 v113, v0
	v_mov_b32_e32 v114, v0
	v_mov_b32_e32 v115, v0
	v_mov_b32_e32 v72, v0
	v_mov_b32_e32 v73, v0
	v_mov_b32_e32 v74, v0
	v_mov_b32_e32 v75, v0
	v_mov_b32_e32 v76, v0
	v_mov_b32_e32 v77, v0
	v_mov_b32_e32 v78, v0
	v_mov_b32_e32 v79, v0
	v_mov_b32_e32 v88, v0
	v_mov_b32_e32 v89, v0
	v_mov_b32_e32 v90, v0
	v_mov_b32_e32 v91, v0
	v_mov_b32_e32 v92, v0
	v_mov_b32_e32 v93, v0
	v_mov_b32_e32 v94, v0
	v_mov_b32_e32 v95, v0
	v_mov_b32_e32 v108, v0
	v_mov_b32_e32 v109, v0
	v_mov_b32_e32 v110, v0
	v_mov_b32_e32 v111, v0
	v_mov_b32_e32 v116, v0
	v_mov_b32_e32 v117, v0
	v_mov_b32_e32 v118, v0
	v_mov_b32_e32 v119, v0
	v_mov_b32_e32 v120, v0
	v_mov_b32_e32 v121, v0
	v_mov_b32_e32 v122, v0
	v_mov_b32_e32 v123, v0
	v_mov_b32_e32 v124, v0
	v_mov_b32_e32 v125, v0
	v_mov_b32_e32 v126, v0
	v_mov_b32_e32 v127, v0
	s_cmp_eq_u32 s68, 1
	s_cbranch_scc1 .LBB0_1584
	s_add_u32 s27, s58, 0xfffc0080
	s_addc_u32 s31, s59, -1
	s_add_i32 s49, 0, 0x10000
	s_cmp_eq_u32 s23, 12
	s_cselect_b32 s63, s55, s31
	s_cselect_b32 s62, s54, s27
	s_cselect_b32 s61, s57, s9
	s_cselect_b32 s60, s56, s8
	s_add_i32 s27, 0, 0x14000
	v_add_u32_e32 v142, s49, v179
	v_add_u32_e32 v170, s27, v179
	ds_read_b128 v[130:133], v142
	ds_read_b128 v[134:137], v142 offset:1024
	ds_read_b128 v[138:141], v142 offset:2048
	ds_read_b128 v[142:145], v142 offset:3072
	ds_read_b128 v[146:149], v170
	ds_read_b128 v[150:153], v170 offset:1024
	ds_read_b128 v[166:169], v170 offset:2048
	ds_read_b128 v[170:173], v170 offset:3072
	v_lshl_add_u64 v[196:197], s[58:59], 0, v[162:163]
	s_add_i32 m0, s1, 0xc000
	ds_read_b128 v[174:177], v186
	ds_read_b128 v[188:191], v186 offset:1024
	ds_read_b128 v[192:195], v186 offset:2048
	ds_read_b128 v[200:203], v186 offset:3072
	ds_read_b128 v[204:207], v186 offset:4096
	ds_read_b128 v[216:219], v186 offset:5120
	ds_read_b128 v[220:223], v186 offset:6144
	ds_read_b128 v[224:227], v186 offset:7168
	global_load_lds_dwordx4 v[196:197], off
	v_lshl_add_u64 v[196:197], s[58:59], 0, v[164:165]
	s_add_i32 m0, s1, 0xe000
	s_nop 0
	global_load_lds_dwordx4 v[196:197], off
	s_waitcnt vmcnt(24)
	s_waitcnt lgkmcnt(0)
	s_barrier
	s_setprio 1
	s_waitcnt lgkmcnt(0)
	v_mfma_f32_16x16x32_bf16 v[124:127], v[130:133], v[174:177], v[124:127]
	v_mfma_f32_16x16x32_bf16 v[120:123], v[138:141], v[174:177], v[120:123]
	v_mfma_f32_16x16x32_bf16 v[116:119], v[130:133], v[192:195], v[116:119]
	v_mfma_f32_16x16x32_bf16 v[108:111], v[138:141], v[192:195], v[108:111]
	v_mfma_f32_16x16x32_bf16 v[92:95], v[130:133], v[204:207], v[92:95]
	v_mfma_f32_16x16x32_bf16 v[88:91], v[138:141], v[204:207], v[88:91]
	v_mfma_f32_16x16x32_bf16 v[76:79], v[130:133], v[220:223], v[76:79]
	v_mfma_f32_16x16x32_bf16 v[72:75], v[138:141], v[220:223], v[72:75]
	v_mfma_f32_16x16x32_bf16 v[124:127], v[134:137], v[188:191], v[124:127]
	v_mfma_f32_16x16x32_bf16 v[120:123], v[142:145], v[188:191], v[120:123]
	v_mfma_f32_16x16x32_bf16 v[116:119], v[134:137], v[200:203], v[116:119]
	v_mfma_f32_16x16x32_bf16 v[108:111], v[142:145], v[200:203], v[108:111]
	v_mfma_f32_16x16x32_bf16 v[92:95], v[134:137], v[216:219], v[92:95]
	v_mfma_f32_16x16x32_bf16 v[88:91], v[142:145], v[216:219], v[88:91]
	v_mfma_f32_16x16x32_bf16 v[76:79], v[134:137], v[224:227], v[76:79]
	v_mfma_f32_16x16x32_bf16 v[72:75], v[142:145], v[224:227], v[72:75]
	s_setprio 0
	s_setprio 1
	v_mfma_f32_16x16x32_bf16 v[112:115], v[146:149], v[174:177], v[112:115]
	v_mfma_f32_16x16x32_bf16 v[104:107], v[166:169], v[174:177], v[104:107]
	v_mfma_f32_16x16x32_bf16 v[100:103], v[146:149], v[192:195], v[100:103]
	v_mfma_f32_16x16x32_bf16 v[96:99], v[166:169], v[192:195], v[96:99]
	v_mfma_f32_16x16x32_bf16 v[84:87], v[146:149], v[204:207], v[84:87]
	v_mfma_f32_16x16x32_bf16 v[80:83], v[166:169], v[204:207], v[80:83]
	v_mfma_f32_16x16x32_bf16 v[68:71], v[146:149], v[220:223], v[68:71]
	v_mfma_f32_16x16x32_bf16 v[64:67], v[166:169], v[220:223], v[64:67]
	v_mfma_f32_16x16x32_bf16 v[112:115], v[150:153], v[188:191], v[112:115]
	v_mfma_f32_16x16x32_bf16 v[104:107], v[170:173], v[188:191], v[104:107]
	v_mfma_f32_16x16x32_bf16 v[100:103], v[150:153], v[200:203], v[100:103]
	v_mfma_f32_16x16x32_bf16 v[96:99], v[170:173], v[200:203], v[96:99]
	v_mfma_f32_16x16x32_bf16 v[84:87], v[150:153], v[216:219], v[84:87]
	v_mfma_f32_16x16x32_bf16 v[80:83], v[170:173], v[216:219], v[80:83]
	v_mfma_f32_16x16x32_bf16 v[68:71], v[150:153], v[224:227], v[68:71]
	v_mfma_f32_16x16x32_bf16 v[64:67], v[170:173], v[224:227], v[64:67]
	s_setprio 0
	s_barrier
	s_add_i32 s31, s49, s0
	v_lshl_add_u64 v[196:197], s[60:61], 0, v[128:129]
	s_mov_b32 m0, s31
	ds_read_b128 v[174:177], v186 offset:16384
	ds_read_b128 v[188:191], v186 offset:17408
	ds_read_b128 v[192:195], v186 offset:18432
	ds_read_b128 v[200:203], v186 offset:19456
	ds_read_b128 v[204:207], v186 offset:20480
	ds_read_b128 v[216:219], v186 offset:21504
	ds_read_b128 v[220:223], v186 offset:22528
	ds_read_b128 v[224:227], v186 offset:23552
	global_load_lds_dwordx4 v[196:197], off
	s_add_i32 m0, s31, 0x2000
	s_add_u32 s70, s60, 0x40000
	v_lshl_add_u64 v[208:209], s[60:61], 0, v[158:159]
	s_addc_u32 s71, s61, 0
	s_add_i32 s27, s27, s0
	global_load_lds_dwordx4 v[208:209], off
	v_lshl_add_u64 v[210:211], s[70:71], 0, v[128:129]
	s_mov_b32 m0, s27
	v_lshl_add_u64 v[214:215], s[62:63], 0, v[156:157]
	global_load_lds_dwordx4 v[210:211], off
	v_lshl_add_u64 v[210:211], s[70:71], 0, v[158:159]
	s_add_i32 m0, s27, 0x2000
	s_nop 0
	global_load_lds_dwordx4 v[210:211], off
	v_lshl_add_u64 v[210:211], s[62:63], 0, v[154:155]
	s_mov_b32 m0, s1
	s_nop 0
	global_load_lds_dwordx4 v[210:211], off
	s_mov_b32 m0, s33
	s_nop 0
	global_load_lds_dwordx4 v[214:215], off
	s_waitcnt vmcnt(24)
	s_waitcnt lgkmcnt(0)
	s_barrier
	s_setprio 1
	s_waitcnt lgkmcnt(0)
	v_mfma_f32_16x16x32_bf16 v[60:63], v[130:133], v[174:177], v[60:63]
	v_mfma_f32_16x16x32_bf16 v[56:59], v[138:141], v[174:177], v[56:59]
	v_mfma_f32_16x16x32_bf16 v[44:47], v[130:133], v[192:195], v[44:47]
	v_mfma_f32_16x16x32_bf16 v[40:43], v[138:141], v[192:195], v[40:43]
	v_mfma_f32_16x16x32_bf16 v[28:31], v[130:133], v[204:207], v[28:31]
	v_mfma_f32_16x16x32_bf16 v[24:27], v[138:141], v[204:207], v[24:27]
	v_mfma_f32_16x16x32_bf16 v[12:15], v[130:133], v[220:223], v[12:15]
	v_mfma_f32_16x16x32_bf16 v[8:11], v[138:141], v[220:223], v[8:11]
	v_mfma_f32_16x16x32_bf16 v[60:63], v[134:137], v[188:191], v[60:63]
	v_mfma_f32_16x16x32_bf16 v[56:59], v[142:145], v[188:191], v[56:59]
	v_mfma_f32_16x16x32_bf16 v[44:47], v[134:137], v[200:203], v[44:47]
	v_mfma_f32_16x16x32_bf16 v[40:43], v[142:145], v[200:203], v[40:43]
	v_mfma_f32_16x16x32_bf16 v[28:31], v[134:137], v[216:219], v[28:31]
	v_mfma_f32_16x16x32_bf16 v[24:27], v[142:145], v[216:219], v[24:27]
	v_mfma_f32_16x16x32_bf16 v[12:15], v[134:137], v[224:227], v[12:15]
	v_mfma_f32_16x16x32_bf16 v[8:11], v[142:145], v[224:227], v[8:11]
	s_setprio 0
	s_setprio 1
	v_mfma_f32_16x16x32_bf16 v[52:55], v[146:149], v[174:177], v[52:55]
	v_mfma_f32_16x16x32_bf16 v[48:51], v[166:169], v[174:177], v[48:51]
	v_mfma_f32_16x16x32_bf16 v[36:39], v[146:149], v[192:195], v[36:39]
	v_mfma_f32_16x16x32_bf16 v[32:35], v[166:169], v[192:195], v[32:35]
	v_mfma_f32_16x16x32_bf16 v[20:23], v[146:149], v[204:207], v[20:23]
	v_mfma_f32_16x16x32_bf16 v[16:19], v[166:169], v[204:207], v[16:19]
	v_mfma_f32_16x16x32_bf16 v[4:7], v[146:149], v[220:223], v[4:7]
	v_mfma_f32_16x16x32_bf16 v[0:3], v[166:169], v[220:223], v[0:3]
	v_mfma_f32_16x16x32_bf16 v[52:55], v[150:153], v[188:191], v[52:55]
	v_mfma_f32_16x16x32_bf16 v[48:51], v[170:173], v[188:191], v[48:51]
	v_mfma_f32_16x16x32_bf16 v[36:39], v[150:153], v[200:203], v[36:39]
	v_mfma_f32_16x16x32_bf16 v[32:35], v[170:173], v[200:203], v[32:35]
	v_mfma_f32_16x16x32_bf16 v[20:23], v[150:153], v[216:219], v[20:23]
	v_mfma_f32_16x16x32_bf16 v[16:19], v[170:173], v[216:219], v[16:19]
	v_mfma_f32_16x16x32_bf16 v[4:7], v[150:153], v[224:227], v[4:7]
	v_mfma_f32_16x16x32_bf16 v[0:3], v[170:173], v[224:227], v[0:3]
	s_setprio 0
	s_barrier
	s_branch .Lp9_mid

.Lp9_mid:
	s_add_i32 s27, 0, 0x18000
	s_add_i32 s31, 0, 0x1c000
	v_add_u32_e32 v142, s27, v179
	v_add_u32_e32 v170, s31, v179
	ds_read_b128 v[130:133], v142
	ds_read_b128 v[134:137], v142 offset:1024
	ds_read_b128 v[138:141], v142 offset:2048
	ds_read_b128 v[142:145], v142 offset:3072
	ds_read_b128 v[146:149], v170
	ds_read_b128 v[150:153], v170 offset:1024
	ds_read_b128 v[166:169], v170 offset:2048
	ds_read_b128 v[170:173], v170 offset:3072
	s_add_u32 s62, s62, 0x40000
	s_addc_u32 s63, s63, 0
	s_mov_b32 m0, s64
	v_lshl_add_u64 v[228:229], s[62:63], 0, v[154:155]
	ds_read_b128 v[174:177], v186 offset:32768
	ds_read_b128 v[188:191], v186 offset:33792
	ds_read_b128 v[192:195], v186 offset:34816
	ds_read_b128 v[200:203], v186 offset:35840
	ds_read_b128 v[204:207], v186 offset:36864
	ds_read_b128 v[216:219], v186 offset:37888
	ds_read_b128 v[220:223], v186 offset:38912
	ds_read_b128 v[224:227], v186 offset:39936
	global_load_lds_dwordx4 v[228:229], off
	v_lshl_add_u64 v[228:229], s[62:63], 0, v[156:157]
	s_mov_b32 m0, s65
	s_nop 0
	global_load_lds_dwordx4 v[228:229], off
	s_waitcnt vmcnt(8)
	s_waitcnt lgkmcnt(0)
	s_barrier
	s_setprio 1
	s_waitcnt lgkmcnt(0)
	v_mfma_f32_16x16x32_bf16 v[124:127], v[130:133], v[174:177], v[124:127]
	v_mfma_f32_16x16x32_bf16 v[120:123], v[138:141], v[174:177], v[120:123]
	v_mfma_f32_16x16x32_bf16 v[116:119], v[130:133], v[192:195], v[116:119]
	v_mfma_f32_16x16x32_bf16 v[108:111], v[138:141], v[192:195], v[108:111]
	v_mfma_f32_16x16x32_bf16 v[92:95], v[130:133], v[204:207], v[92:95]
	v_mfma_f32_16x16x32_bf16 v[88:91], v[138:141], v[204:207], v[88:91]
	v_mfma_f32_16x16x32_bf16 v[76:79], v[130:133], v[220:223], v[76:79]
	v_mfma_f32_16x16x32_bf16 v[72:75], v[138:141], v[220:223], v[72:75]
	v_mfma_f32_16x16x32_bf16 v[124:127], v[134:137], v[188:191], v[124:127]
	v_mfma_f32_16x16x32_bf16 v[120:123], v[142:145], v[188:191], v[120:123]
	v_mfma_f32_16x16x32_bf16 v[116:119], v[134:137], v[200:203], v[116:119]
	v_mfma_f32_16x16x32_bf16 v[108:111], v[142:145], v[200:203], v[108:111]
	v_mfma_f32_16x16x32_bf16 v[92:95], v[134:137], v[216:219], v[92:95]
	v_mfma_f32_16x16x32_bf16 v[88:91], v[142:145], v[216:219], v[88:91]
	v_mfma_f32_16x16x32_bf16 v[76:79], v[134:137], v[224:227], v[76:79]
	v_mfma_f32_16x16x32_bf16 v[72:75], v[142:145], v[224:227], v[72:75]
	s_setprio 0
	s_setprio 1
	v_mfma_f32_16x16x32_bf16 v[112:115], v[146:149], v[174:177], v[112:115]
	v_mfma_f32_16x16x32_bf16 v[104:107], v[166:169], v[174:177], v[104:107]
	v_mfma_f32_16x16x32_bf16 v[100:103], v[146:149], v[192:195], v[100:103]
	v_mfma_f32_16x16x32_bf16 v[96:99], v[166:169], v[192:195], v[96:99]
	v_mfma_f32_16x16x32_bf16 v[84:87], v[146:149], v[204:207], v[84:87]
	v_mfma_f32_16x16x32_bf16 v[80:83], v[166:169], v[204:207], v[80:83]
	v_mfma_f32_16x16x32_bf16 v[68:71], v[146:149], v[220:223], v[68:71]
	v_mfma_f32_16x16x32_bf16 v[64:67], v[166:169], v[220:223], v[64:67]
	v_mfma_f32_16x16x32_bf16 v[112:115], v[150:153], v[188:191], v[112:115]
	v_mfma_f32_16x16x32_bf16 v[104:107], v[170:173], v[188:191], v[104:107]
	v_mfma_f32_16x16x32_bf16 v[100:103], v[150:153], v[200:203], v[100:103]
	v_mfma_f32_16x16x32_bf16 v[96:99], v[170:173], v[200:203], v[96:99]
	v_mfma_f32_16x16x32_bf16 v[84:87], v[150:153], v[216:219], v[84:87]
	v_mfma_f32_16x16x32_bf16 v[80:83], v[170:173], v[216:219], v[80:83]
	v_mfma_f32_16x16x32_bf16 v[68:71], v[150:153], v[224:227], v[68:71]
	v_mfma_f32_16x16x32_bf16 v[64:67], v[170:173], v[224:227], v[64:67]
	s_setprio 0
	s_barrier
	s_add_i32 s27, s27, s0
	v_lshl_add_u64 v[196:197], v[196:197], 0, s[88:89]
	s_mov_b32 m0, s27
	ds_read_b128 v[174:177], v186 offset:49152
	ds_read_b128 v[188:191], v186 offset:50176
	ds_read_b128 v[192:195], v186 offset:51200
	ds_read_b128 v[200:203], v186 offset:52224
	ds_read_b128 v[204:207], v186 offset:53248
	ds_read_b128 v[216:219], v186 offset:54272
	ds_read_b128 v[220:223], v186 offset:55296
	ds_read_b128 v[224:227], v186 offset:56320
	global_load_lds_dwordx4 v[196:197], off
	s_add_i32 m0, s27, 0x2000
	s_add_u32 s60, s60, 0x40080
	v_lshl_add_u64 v[196:197], v[208:209], 0, s[88:89]
	s_addc_u32 s61, s61, 0
	s_add_i32 s27, s31, s0
	global_load_lds_dwordx4 v[196:197], off
	v_lshl_add_u64 v[196:197], s[60:61], 0, v[128:129]
	s_mov_b32 m0, s27
	s_nop 0
	global_load_lds_dwordx4 v[196:197], off
	v_lshl_add_u64 v[196:197], s[60:61], 0, v[158:159]
	s_add_i32 m0, s27, 0x2000
	s_nop 0
	global_load_lds_dwordx4 v[196:197], off
	v_lshl_add_u64 v[196:197], v[210:211], 0, s[88:89]
	s_mov_b32 m0, s66
	s_nop 0
	global_load_lds_dwordx4 v[196:197], off
	v_lshl_add_u64 v[196:197], v[214:215], 0, s[88:89]
	s_mov_b32 m0, s67
	s_nop 0
	global_load_lds_dwordx4 v[196:197], off
	s_waitcnt vmcnt(8)
	s_waitcnt lgkmcnt(0)
	s_barrier
	s_setprio 1
	s_waitcnt lgkmcnt(0)
	v_mfma_f32_16x16x32_bf16 v[60:63], v[130:133], v[174:177], v[60:63]
	v_mfma_f32_16x16x32_bf16 v[56:59], v[138:141], v[174:177], v[56:59]
	v_mfma_f32_16x16x32_bf16 v[44:47], v[130:133], v[192:195], v[44:47]
	v_mfma_f32_16x16x32_bf16 v[40:43], v[138:141], v[192:195], v[40:43]
	v_mfma_f32_16x16x32_bf16 v[28:31], v[130:133], v[204:207], v[28:31]
	v_mfma_f32_16x16x32_bf16 v[24:27], v[138:141], v[204:207], v[24:27]
	v_mfma_f32_16x16x32_bf16 v[12:15], v[130:133], v[220:223], v[12:15]
	v_mfma_f32_16x16x32_bf16 v[8:11], v[138:141], v[220:223], v[8:11]
	v_mfma_f32_16x16x32_bf16 v[60:63], v[134:137], v[188:191], v[60:63]
	v_mfma_f32_16x16x32_bf16 v[56:59], v[142:145], v[188:191], v[56:59]
	v_mfma_f32_16x16x32_bf16 v[44:47], v[134:137], v[200:203], v[44:47]
	v_mfma_f32_16x16x32_bf16 v[40:43], v[142:145], v[200:203], v[40:43]
	v_mfma_f32_16x16x32_bf16 v[28:31], v[134:137], v[216:219], v[28:31]
	v_mfma_f32_16x16x32_bf16 v[24:27], v[142:145], v[216:219], v[24:27]
	v_mfma_f32_16x16x32_bf16 v[12:15], v[134:137], v[224:227], v[12:15]
	v_mfma_f32_16x16x32_bf16 v[8:11], v[142:145], v[224:227], v[8:11]
	s_setprio 0
	s_setprio 1
	v_mfma_f32_16x16x32_bf16 v[52:55], v[146:149], v[174:177], v[52:55]
	v_mfma_f32_16x16x32_bf16 v[48:51], v[166:169], v[174:177], v[48:51]
	v_mfma_f32_16x16x32_bf16 v[36:39], v[146:149], v[192:195], v[36:39]
	v_mfma_f32_16x16x32_bf16 v[32:35], v[166:169], v[192:195], v[32:35]
	v_mfma_f32_16x16x32_bf16 v[20:23], v[146:149], v[204:207], v[20:23]
	v_mfma_f32_16x16x32_bf16 v[16:19], v[166:169], v[204:207], v[16:19]
	v_mfma_f32_16x16x32_bf16 v[4:7], v[146:149], v[220:223], v[4:7]
	v_mfma_f32_16x16x32_bf16 v[0:3], v[166:169], v[220:223], v[0:3]
	v_mfma_f32_16x16x32_bf16 v[52:55], v[150:153], v[188:191], v[52:55]
	v_mfma_f32_16x16x32_bf16 v[48:51], v[170:173], v[188:191], v[48:51]
	v_mfma_f32_16x16x32_bf16 v[36:39], v[150:153], v[200:203], v[36:39]
	v_mfma_f32_16x16x32_bf16 v[32:35], v[170:173], v[200:203], v[32:35]
	v_mfma_f32_16x16x32_bf16 v[20:23], v[150:153], v[216:219], v[20:23]
	v_mfma_f32_16x16x32_bf16 v[16:19], v[170:173], v[216:219], v[16:19]
	v_mfma_f32_16x16x32_bf16 v[4:7], v[150:153], v[224:227], v[4:7]
	v_mfma_f32_16x16x32_bf16 v[0:3], v[170:173], v[224:227], v[0:3]
	s_setprio 0
	s_barrier
	s_add_i32 s23, s23, 2
	s_add_u32 s58, s58, 0x100
	s_addc_u32 s59, s59, 0
	s_add_u32 s8, s8, 0x100
	s_addc_u32 s9, s9, 0
	s_cmp_gt_u32 s23, 13
	s_cbranch_scc0 .LBB0_1584
	s_and_b64 vcc, exec, s[46:47]
	s_cbranch_vccz .LBB0_1587
	s_barrier

.LBB0_1688:
	s_or_b64 exec, exec, s[48:49]
	s_ashr_i32 s45, s44, 31
	s_lshl_b64 s[48:49], s[44:45], 19
	s_add_u32 s48, s80, s48
	s_addc_u32 s49, s81, s49
	s_and_b64 s[50:51], s[42:43], exec
	s_cselect_b32 s45, s49, s55
	s_cselect_b32 s53, s48, s54
	s_ashr_i32 s47, s46, 31
	s_lshl_b64 s[50:51], s[46:47], 19
	s_add_u32 s50, s22, s50
	s_addc_u32 s51, s23, s51
	s_and_b64 s[58:59], s[42:43], exec
	s_cselect_b32 s47, s51, s57
	s_cselect_b32 s65, s50, s56
	s_add_u32 s54, s54, 0x40080
	s_addc_u32 s55, s55, 0
	s_add_u32 s66, s56, 0x100
	v_mov_b32_e32 v0, 0
	s_addc_u32 s67, s57, 0
	s_mov_b32 s68, -2
	v_mov_b32_e32 v1, v0
	v_mov_b32_e32 v2, v0
	v_mov_b32_e32 v3, v0
	v_mov_b32_e32 v4, v0
	v_mov_b32_e32 v5, v0
	v_mov_b32_e32 v6, v0
	v_mov_b32_e32 v7, v0
	v_mov_b32_e32 v16, v0
	v_mov_b32_e32 v17, v0
	v_mov_b32_e32 v18, v0
	v_mov_b32_e32 v19, v0
	v_mov_b32_e32 v20, v0
	v_mov_b32_e32 v21, v0
	v_mov_b32_e32 v22, v0
	v_mov_b32_e32 v23, v0
	v_mov_b32_e32 v32, v0
	v_mov_b32_e32 v33, v0
	v_mov_b32_e32 v34, v0
	v_mov_b32_e32 v35, v0
	v_mov_b32_e32 v36, v0
	v_mov_b32_e32 v37, v0
	v_mov_b32_e32 v38, v0
	v_mov_b32_e32 v39, v0
	v_mov_b32_e32 v48, v0
	v_mov_b32_e32 v49, v0
	v_mov_b32_e32 v50, v0
	v_mov_b32_e32 v51, v0
	v_mov_b32_e32 v52, v0
	v_mov_b32_e32 v53, v0
	v_mov_b32_e32 v54, v0
	v_mov_b32_e32 v55, v0
	v_mov_b32_e32 v8, v0
	v_mov_b32_e32 v9, v0
	v_mov_b32_e32 v10, v0
	v_mov_b32_e32 v11, v0
	v_mov_b32_e32 v12, v0
	v_mov_b32_e32 v13, v0
	v_mov_b32_e32 v14, v0
	v_mov_b32_e32 v15, v0
	v_mov_b32_e32 v24, v0
	v_mov_b32_e32 v25, v0
	v_mov_b32_e32 v26, v0
	v_mov_b32_e32 v27, v0
	v_mov_b32_e32 v28, v0
	v_mov_b32_e32 v29, v0
	v_mov_b32_e32 v30, v0
	v_mov_b32_e32 v31, v0
	v_mov_b32_e32 v40, v0
	v_mov_b32_e32 v41, v0
	v_mov_b32_e32 v42, v0
	v_mov_b32_e32 v43, v0
	v_mov_b32_e32 v44, v0
	v_mov_b32_e32 v45, v0
	v_mov_b32_e32 v46, v0
	v_mov_b32_e32 v47, v0
	v_mov_b32_e32 v56, v0
	v_mov_b32_e32 v57, v0
	v_mov_b32_e32 v58, v0
	v_mov_b32_e32 v59, v0
	v_mov_b32_e32 v60, v0
	v_mov_b32_e32 v61, v0
	v_mov_b32_e32 v62, v0
	v_mov_b32_e32 v63, v0
	v_mov_b32_e32 v64, v0
	v_mov_b32_e32 v65, v0
	v_mov_b32_e32 v66, v0
	v_mov_b32_e32 v67, v0
	v_mov_b32_e32 v68, v0
	v_mov_b32_e32 v69, v0
	v_mov_b32_e32 v70, v0
	v_mov_b32_e32 v71, v0
	v_mov_b32_e32 v80, v0
	v_mov_b32_e32 v81, v0
	v_mov_b32_e32 v82, v0
	v_mov_b32_e32 v83, v0
	v_mov_b32_e32 v84, v0
	v_mov_b32_e32 v85, v0
	v_mov_b32_e32 v86, v0
	v_mov_b32_e32 v87, v0
	v_mov_b32_e32 v96, v0
	v_mov_b32_e32 v97, v0
	v_mov_b32_e32 v98, v0
	v_mov_b32_e32 v99, v0
	v_mov_b32_e32 v100, v0
	v_mov_b32_e32 v101, v0
	v_mov_b32_e32 v102, v0
	v_mov_b32_e32 v103, v0
	v_mov_b32_e32 v112, v0
	v_mov_b32_e32 v113, v0
	v_mov_b32_e32 v114, v0
	v_mov_b32_e32 v115, v0
	v_mov_b32_e32 v116, v0
	v_mov_b32_e32 v117, v0
	v_mov_b32_e32 v118, v0
	v_mov_b32_e32 v119, v0
	v_mov_b32_e32 v72, v0
	v_mov_b32_e32 v73, v0
	v_mov_b32_e32 v74, v0
	v_mov_b32_e32 v75, v0
	v_mov_b32_e32 v76, v0
	v_mov_b32_e32 v77, v0
	v_mov_b32_e32 v78, v0
	v_mov_b32_e32 v79, v0
	v_mov_b32_e32 v88, v0
	v_mov_b32_e32 v89, v0
	v_mov_b32_e32 v90, v0
	v_mov_b32_e32 v91, v0
	v_mov_b32_e32 v92, v0
	v_mov_b32_e32 v93, v0
	v_mov_b32_e32 v94, v0
	v_mov_b32_e32 v95, v0
	v_mov_b32_e32 v104, v0
	v_mov_b32_e32 v105, v0
	v_mov_b32_e32 v106, v0
	v_mov_b32_e32 v107, v0
	v_mov_b32_e32 v108, v0
	v_mov_b32_e32 v109, v0
	v_mov_b32_e32 v110, v0
	v_mov_b32_e32 v111, v0
	v_mov_b32_e32 v120, v0
	v_mov_b32_e32 v121, v0
	v_mov_b32_e32 v122, v0
	v_mov_b32_e32 v123, v0
	v_mov_b32_e32 v124, v0
	v_mov_b32_e32 v125, v0
	v_mov_b32_e32 v126, v0
	v_mov_b32_e32 v127, v0
	s_cmp_eq_u32 s9, 0
	s_cbranch_scc1 .LBB0_1689
	s_add_u32 s56, s54, 0xfffc0080
	s_addc_u32 s57, s55, -1
	s_add_i32 s69, 0, 0x10000
	s_cmp_eq_u32 s68, 12
	s_cselect_b32 s59, s45, s57
	s_cselect_b32 s58, s53, s56
	v_add_u32_e32 v146, s69, v149
	s_cselect_b32 s57, s47, s67
	s_cselect_b32 s56, s65, s66
	s_add_i32 s72, 0, 0x14000
	ds_read_b128 v[142:145], v146
	ds_read_b128 v[154:157], v146 offset:1024
	ds_read_b128 v[158:161], v146 offset:2048
	ds_read_b128 v[162:165], v146 offset:3072
	v_add_u32_e32 v146, s72, v149
	ds_read_b128 v[166:169], v146
	ds_read_b128 v[170:173], v146 offset:1024
	ds_read_b128 v[174:177], v146 offset:2048
	ds_read_b128 v[178:181], v146 offset:3072
	v_lshl_add_u64 v[146:147], s[54:55], 0, v[138:139]
	s_add_i32 m0, s1, 0xc000
	ds_read_b128 v[182:185], v153
	ds_read_b128 v[186:189], v153 offset:1024
	ds_read_b128 v[190:193], v153 offset:2048
	ds_read_b128 v[194:197], v153 offset:3072
	ds_read_b128 v[200:203], v153 offset:4096
	ds_read_b128 v[204:207], v153 offset:5120
	ds_read_b128 v[216:219], v153 offset:6144
	ds_read_b128 v[220:223], v153 offset:7168
	global_load_lds_dwordx4 v[146:147], off
	v_lshl_add_u64 v[146:147], s[54:55], 0, v[140:141]
	s_add_i32 m0, s1, 0xe000
	s_nop 0
	global_load_lds_dwordx4 v[146:147], off
	s_waitcnt vmcnt(24)
	s_waitcnt lgkmcnt(0)
	s_barrier
	s_setprio 1
	s_waitcnt lgkmcnt(0)
	v_mfma_f32_16x16x32_bf16 v[124:127], v[142:145], v[182:185], v[124:127]
	v_mfma_f32_16x16x32_bf16 v[120:123], v[158:161], v[182:185], v[120:123]
	v_mfma_f32_16x16x32_bf16 v[108:111], v[142:145], v[190:193], v[108:111]
	v_mfma_f32_16x16x32_bf16 v[104:107], v[158:161], v[190:193], v[104:107]
	v_mfma_f32_16x16x32_bf16 v[92:95], v[142:145], v[200:203], v[92:95]
	v_mfma_f32_16x16x32_bf16 v[88:91], v[158:161], v[200:203], v[88:91]
	v_mfma_f32_16x16x32_bf16 v[76:79], v[142:145], v[216:219], v[76:79]
	v_mfma_f32_16x16x32_bf16 v[72:75], v[158:161], v[216:219], v[72:75]
	v_mfma_f32_16x16x32_bf16 v[124:127], v[154:157], v[186:189], v[124:127]
	v_mfma_f32_16x16x32_bf16 v[120:123], v[162:165], v[186:189], v[120:123]
	v_mfma_f32_16x16x32_bf16 v[108:111], v[154:157], v[194:197], v[108:111]
	v_mfma_f32_16x16x32_bf16 v[104:107], v[162:165], v[194:197], v[104:107]
	v_mfma_f32_16x16x32_bf16 v[92:95], v[154:157], v[204:207], v[92:95]
	v_mfma_f32_16x16x32_bf16 v[88:91], v[162:165], v[204:207], v[88:91]
	v_mfma_f32_16x16x32_bf16 v[76:79], v[154:157], v[220:223], v[76:79]
	v_mfma_f32_16x16x32_bf16 v[72:75], v[162:165], v[220:223], v[72:75]
	s_setprio 0
	s_setprio 1
	v_mfma_f32_16x16x32_bf16 v[116:119], v[166:169], v[182:185], v[116:119]
	v_mfma_f32_16x16x32_bf16 v[112:115], v[174:177], v[182:185], v[112:115]
	v_mfma_f32_16x16x32_bf16 v[100:103], v[166:169], v[190:193], v[100:103]
	v_mfma_f32_16x16x32_bf16 v[96:99], v[174:177], v[190:193], v[96:99]
	v_mfma_f32_16x16x32_bf16 v[84:87], v[166:169], v[200:203], v[84:87]
	v_mfma_f32_16x16x32_bf16 v[80:83], v[174:177], v[200:203], v[80:83]
	v_mfma_f32_16x16x32_bf16 v[68:71], v[166:169], v[216:219], v[68:71]
	v_mfma_f32_16x16x32_bf16 v[64:67], v[174:177], v[216:219], v[64:67]
	v_mfma_f32_16x16x32_bf16 v[116:119], v[170:173], v[186:189], v[116:119]
	v_mfma_f32_16x16x32_bf16 v[112:115], v[178:181], v[186:189], v[112:115]
	v_mfma_f32_16x16x32_bf16 v[100:103], v[170:173], v[194:197], v[100:103]
	v_mfma_f32_16x16x32_bf16 v[96:99], v[178:181], v[194:197], v[96:99]
	v_mfma_f32_16x16x32_bf16 v[84:87], v[170:173], v[204:207], v[84:87]
	v_mfma_f32_16x16x32_bf16 v[80:83], v[178:181], v[204:207], v[80:83]
	v_mfma_f32_16x16x32_bf16 v[68:71], v[170:173], v[220:223], v[68:71]
	v_mfma_f32_16x16x32_bf16 v[64:67], v[178:181], v[220:223], v[64:67]
	s_setprio 0
	s_barrier
	s_add_i32 s69, s69, s0
	v_lshl_add_u64 v[146:147], s[56:57], 0, v[128:129]
	s_mov_b32 m0, s69
	ds_read_b128 v[182:185], v153 offset:16384
	ds_read_b128 v[186:189], v153 offset:17408
	ds_read_b128 v[190:193], v153 offset:18432
	ds_read_b128 v[194:197], v153 offset:19456
	ds_read_b128 v[200:203], v153 offset:20480
	ds_read_b128 v[204:207], v153 offset:21504
	ds_read_b128 v[216:219], v153 offset:22528
	ds_read_b128 v[220:223], v153 offset:23552
	global_load_lds_dwordx4 v[146:147], off
	s_add_i32 m0, s69, 0x2000
	s_add_u32 s70, s56, 0x40000
	v_lshl_add_u64 v[208:209], s[56:57], 0, v[134:135]
	s_addc_u32 s71, s57, 0
	s_add_i32 s69, s72, s0
	global_load_lds_dwordx4 v[208:209], off
	v_lshl_add_u64 v[210:211], s[70:71], 0, v[128:129]
	s_mov_b32 m0, s69
	v_lshl_add_u64 v[214:215], s[58:59], 0, v[132:133]
	global_load_lds_dwordx4 v[210:211], off
	v_lshl_add_u64 v[210:211], s[70:71], 0, v[134:135]
	s_add_i32 m0, s69, 0x2000
	s_nop 0
	global_load_lds_dwordx4 v[210:211], off
	v_lshl_add_u64 v[210:211], s[58:59], 0, v[130:131]
	s_mov_b32 m0, s1
	s_nop 0
	global_load_lds_dwordx4 v[210:211], off
	s_mov_b32 m0, s33
	s_nop 0
	global_load_lds_dwordx4 v[214:215], off
	s_waitcnt vmcnt(24)
	s_waitcnt lgkmcnt(0)
	s_barrier
	s_setprio 1
	s_waitcnt lgkmcnt(0)
	v_mfma_f32_16x16x32_bf16 v[60:63], v[142:145], v[182:185], v[60:63]
	v_mfma_f32_16x16x32_bf16 v[56:59], v[158:161], v[182:185], v[56:59]
	v_mfma_f32_16x16x32_bf16 v[44:47], v[142:145], v[190:193], v[44:47]
	v_mfma_f32_16x16x32_bf16 v[40:43], v[158:161], v[190:193], v[40:43]
	v_mfma_f32_16x16x32_bf16 v[28:31], v[142:145], v[200:203], v[28:31]
	v_mfma_f32_16x16x32_bf16 v[24:27], v[158:161], v[200:203], v[24:27]
	v_mfma_f32_16x16x32_bf16 v[12:15], v[142:145], v[216:219], v[12:15]
	v_mfma_f32_16x16x32_bf16 v[8:11], v[158:161], v[216:219], v[8:11]
	v_mfma_f32_16x16x32_bf16 v[60:63], v[154:157], v[186:189], v[60:63]
	v_mfma_f32_16x16x32_bf16 v[56:59], v[162:165], v[186:189], v[56:59]
	v_mfma_f32_16x16x32_bf16 v[44:47], v[154:157], v[194:197], v[44:47]
	v_mfma_f32_16x16x32_bf16 v[40:43], v[162:165], v[194:197], v[40:43]
	v_mfma_f32_16x16x32_bf16 v[28:31], v[154:157], v[204:207], v[28:31]
	v_mfma_f32_16x16x32_bf16 v[24:27], v[162:165], v[204:207], v[24:27]
	v_mfma_f32_16x16x32_bf16 v[12:15], v[154:157], v[220:223], v[12:15]
	v_mfma_f32_16x16x32_bf16 v[8:11], v[162:165], v[220:223], v[8:11]
	s_setprio 0
	s_setprio 1
	v_mfma_f32_16x16x32_bf16 v[52:55], v[166:169], v[182:185], v[52:55]
	v_mfma_f32_16x16x32_bf16 v[48:51], v[174:177], v[182:185], v[48:51]
	v_mfma_f32_16x16x32_bf16 v[36:39], v[166:169], v[190:193], v[36:39]
	v_mfma_f32_16x16x32_bf16 v[32:35], v[174:177], v[190:193], v[32:35]
	v_mfma_f32_16x16x32_bf16 v[20:23], v[166:169], v[200:203], v[20:23]
	v_mfma_f32_16x16x32_bf16 v[16:19], v[174:177], v[200:203], v[16:19]
	v_mfma_f32_16x16x32_bf16 v[4:7], v[166:169], v[216:219], v[4:7]
	v_mfma_f32_16x16x32_bf16 v[0:3], v[174:177], v[216:219], v[0:3]
	v_mfma_f32_16x16x32_bf16 v[52:55], v[170:173], v[186:189], v[52:55]
	v_mfma_f32_16x16x32_bf16 v[48:51], v[178:181], v[186:189], v[48:51]
	v_mfma_f32_16x16x32_bf16 v[36:39], v[170:173], v[194:197], v[36:39]
	v_mfma_f32_16x16x32_bf16 v[32:35], v[178:181], v[194:197], v[32:35]
	v_mfma_f32_16x16x32_bf16 v[20:23], v[170:173], v[204:207], v[20:23]
	v_mfma_f32_16x16x32_bf16 v[16:19], v[178:181], v[204:207], v[16:19]
	v_mfma_f32_16x16x32_bf16 v[4:7], v[170:173], v[220:223], v[4:7]
	v_mfma_f32_16x16x32_bf16 v[0:3], v[178:181], v[220:223], v[0:3]
	s_setprio 0
	s_barrier
	s_branch .Lmlp1_mid

.Lmlp1_mid:
	s_add_i32 s69, 0, 0x18000
	s_add_i32 s70, 0, 0x1c000
	v_add_u32_e32 v162, s69, v149
	v_add_u32_e32 v178, s70, v149
	ds_read_b128 v[142:145], v162
	ds_read_b128 v[154:157], v162 offset:1024
	ds_read_b128 v[158:161], v162 offset:2048
	ds_read_b128 v[162:165], v162 offset:3072
	ds_read_b128 v[166:169], v178
	ds_read_b128 v[170:173], v178 offset:1024
	ds_read_b128 v[174:177], v178 offset:2048
	ds_read_b128 v[178:181], v178 offset:3072
	s_add_u32 s58, s58, 0x40000
	s_addc_u32 s59, s59, 0
	s_mov_b32 m0, s60
	v_lshl_add_u64 v[224:225], s[58:59], 0, v[130:131]
	ds_read_b128 v[182:185], v153 offset:32768
	ds_read_b128 v[186:189], v153 offset:33792
	ds_read_b128 v[190:193], v153 offset:34816
	ds_read_b128 v[194:197], v153 offset:35840
	ds_read_b128 v[200:203], v153 offset:36864
	ds_read_b128 v[204:207], v153 offset:37888
	ds_read_b128 v[216:219], v153 offset:38912
	ds_read_b128 v[220:223], v153 offset:39936
	global_load_lds_dwordx4 v[224:225], off
	v_lshl_add_u64 v[224:225], s[58:59], 0, v[132:133]
	s_mov_b32 m0, s61
	s_nop 0
	global_load_lds_dwordx4 v[224:225], off
	s_waitcnt vmcnt(8)
	s_waitcnt lgkmcnt(0)
	s_barrier
	s_setprio 1
	s_waitcnt lgkmcnt(0)
	v_mfma_f32_16x16x32_bf16 v[124:127], v[142:145], v[182:185], v[124:127]
	v_mfma_f32_16x16x32_bf16 v[120:123], v[158:161], v[182:185], v[120:123]
	v_mfma_f32_16x16x32_bf16 v[108:111], v[142:145], v[190:193], v[108:111]
	v_mfma_f32_16x16x32_bf16 v[104:107], v[158:161], v[190:193], v[104:107]
	v_mfma_f32_16x16x32_bf16 v[92:95], v[142:145], v[200:203], v[92:95]
	v_mfma_f32_16x16x32_bf16 v[88:91], v[158:161], v[200:203], v[88:91]
	v_mfma_f32_16x16x32_bf16 v[76:79], v[142:145], v[216:219], v[76:79]
	v_mfma_f32_16x16x32_bf16 v[72:75], v[158:161], v[216:219], v[72:75]
	v_mfma_f32_16x16x32_bf16 v[124:127], v[154:157], v[186:189], v[124:127]
	v_mfma_f32_16x16x32_bf16 v[120:123], v[162:165], v[186:189], v[120:123]
	v_mfma_f32_16x16x32_bf16 v[108:111], v[154:157], v[194:197], v[108:111]
	v_mfma_f32_16x16x32_bf16 v[104:107], v[162:165], v[194:197], v[104:107]
	v_mfma_f32_16x16x32_bf16 v[92:95], v[154:157], v[204:207], v[92:95]
	v_mfma_f32_16x16x32_bf16 v[88:91], v[162:165], v[204:207], v[88:91]
	v_mfma_f32_16x16x32_bf16 v[76:79], v[154:157], v[220:223], v[76:79]
	v_mfma_f32_16x16x32_bf16 v[72:75], v[162:165], v[220:223], v[72:75]
	s_setprio 0
	s_setprio 1
	v_mfma_f32_16x16x32_bf16 v[116:119], v[166:169], v[182:185], v[116:119]
	v_mfma_f32_16x16x32_bf16 v[112:115], v[174:177], v[182:185], v[112:115]
	v_mfma_f32_16x16x32_bf16 v[100:103], v[166:169], v[190:193], v[100:103]
	v_mfma_f32_16x16x32_bf16 v[96:99], v[174:177], v[190:193], v[96:99]
	v_mfma_f32_16x16x32_bf16 v[84:87], v[166:169], v[200:203], v[84:87]
	v_mfma_f32_16x16x32_bf16 v[80:83], v[174:177], v[200:203], v[80:83]
	v_mfma_f32_16x16x32_bf16 v[68:71], v[166:169], v[216:219], v[68:71]
	v_mfma_f32_16x16x32_bf16 v[64:67], v[174:177], v[216:219], v[64:67]
	v_mfma_f32_16x16x32_bf16 v[116:119], v[170:173], v[186:189], v[116:119]
	v_mfma_f32_16x16x32_bf16 v[112:115], v[178:181], v[186:189], v[112:115]
	v_mfma_f32_16x16x32_bf16 v[100:103], v[170:173], v[194:197], v[100:103]
	v_mfma_f32_16x16x32_bf16 v[96:99], v[178:181], v[194:197], v[96:99]
	v_mfma_f32_16x16x32_bf16 v[84:87], v[170:173], v[204:207], v[84:87]
	v_mfma_f32_16x16x32_bf16 v[80:83], v[178:181], v[204:207], v[80:83]
	v_mfma_f32_16x16x32_bf16 v[68:71], v[170:173], v[220:223], v[68:71]
	v_mfma_f32_16x16x32_bf16 v[64:67], v[178:181], v[220:223], v[64:67]
	s_setprio 0
	s_barrier
	s_add_i32 s58, s69, s0
	v_lshl_add_u64 v[146:147], v[146:147], 0, s[88:89]
	s_mov_b32 m0, s58
	ds_read_b128 v[182:185], v153 offset:49152
	ds_read_b128 v[186:189], v153 offset:50176
	ds_read_b128 v[190:193], v153 offset:51200
	ds_read_b128 v[194:197], v153 offset:52224
	ds_read_b128 v[200:203], v153 offset:53248
	ds_read_b128 v[204:207], v153 offset:54272
	ds_read_b128 v[216:219], v153 offset:55296
	ds_read_b128 v[220:223], v153 offset:56320
	global_load_lds_dwordx4 v[146:147], off
	s_add_i32 m0, s58, 0x2000
	s_add_u32 s56, s56, 0x40080
	v_lshl_add_u64 v[146:147], v[208:209], 0, s[88:89]
	s_addc_u32 s57, s57, 0
	s_add_i32 s58, s70, s0
	global_load_lds_dwordx4 v[146:147], off
	v_lshl_add_u64 v[146:147], s[56:57], 0, v[128:129]
	s_mov_b32 m0, s58
	s_nop 0
	global_load_lds_dwordx4 v[146:147], off
	v_lshl_add_u64 v[146:147], s[56:57], 0, v[134:135]
	s_add_i32 m0, s58, 0x2000
	s_nop 0
	global_load_lds_dwordx4 v[146:147], off
	v_lshl_add_u64 v[146:147], v[210:211], 0, s[88:89]
	s_mov_b32 m0, s62
	s_nop 0
	global_load_lds_dwordx4 v[146:147], off
	v_lshl_add_u64 v[146:147], v[214:215], 0, s[88:89]
	s_mov_b32 m0, s63
	s_nop 0
	global_load_lds_dwordx4 v[146:147], off
	s_waitcnt vmcnt(8)
	s_waitcnt lgkmcnt(0)
	s_barrier
	s_setprio 1
	s_waitcnt lgkmcnt(0)
	v_mfma_f32_16x16x32_bf16 v[60:63], v[142:145], v[182:185], v[60:63]
	v_mfma_f32_16x16x32_bf16 v[56:59], v[158:161], v[182:185], v[56:59]
	v_mfma_f32_16x16x32_bf16 v[44:47], v[142:145], v[190:193], v[44:47]
	v_mfma_f32_16x16x32_bf16 v[40:43], v[158:161], v[190:193], v[40:43]
	v_mfma_f32_16x16x32_bf16 v[28:31], v[142:145], v[200:203], v[28:31]
	v_mfma_f32_16x16x32_bf16 v[24:27], v[158:161], v[200:203], v[24:27]
	v_mfma_f32_16x16x32_bf16 v[12:15], v[142:145], v[216:219], v[12:15]
	v_mfma_f32_16x16x32_bf16 v[8:11], v[158:161], v[216:219], v[8:11]
	v_mfma_f32_16x16x32_bf16 v[60:63], v[154:157], v[186:189], v[60:63]
	v_mfma_f32_16x16x32_bf16 v[56:59], v[162:165], v[186:189], v[56:59]
	v_mfma_f32_16x16x32_bf16 v[44:47], v[154:157], v[194:197], v[44:47]
	v_mfma_f32_16x16x32_bf16 v[40:43], v[162:165], v[194:197], v[40:43]
	v_mfma_f32_16x16x32_bf16 v[28:31], v[154:157], v[204:207], v[28:31]
	v_mfma_f32_16x16x32_bf16 v[24:27], v[162:165], v[204:207], v[24:27]
	v_mfma_f32_16x16x32_bf16 v[12:15], v[154:157], v[220:223], v[12:15]
	v_mfma_f32_16x16x32_bf16 v[8:11], v[162:165], v[220:223], v[8:11]
	s_setprio 0
	s_setprio 1
	v_mfma_f32_16x16x32_bf16 v[52:55], v[166:169], v[182:185], v[52:55]
	v_mfma_f32_16x16x32_bf16 v[48:51], v[174:177], v[182:185], v[48:51]
	v_mfma_f32_16x16x32_bf16 v[36:39], v[166:169], v[190:193], v[36:39]
	v_mfma_f32_16x16x32_bf16 v[32:35], v[174:177], v[190:193], v[32:35]
	v_mfma_f32_16x16x32_bf16 v[20:23], v[166:169], v[200:203], v[20:23]
	v_mfma_f32_16x16x32_bf16 v[16:19], v[174:177], v[200:203], v[16:19]
	v_mfma_f32_16x16x32_bf16 v[4:7], v[166:169], v[216:219], v[4:7]
	v_mfma_f32_16x16x32_bf16 v[0:3], v[174:177], v[216:219], v[0:3]
	v_mfma_f32_16x16x32_bf16 v[52:55], v[170:173], v[186:189], v[52:55]
	v_mfma_f32_16x16x32_bf16 v[48:51], v[178:181], v[186:189], v[48:51]
	v_mfma_f32_16x16x32_bf16 v[36:39], v[170:173], v[194:197], v[36:39]
	v_mfma_f32_16x16x32_bf16 v[32:35], v[178:181], v[194:197], v[32:35]
	v_mfma_f32_16x16x32_bf16 v[20:23], v[170:173], v[204:207], v[20:23]
	v_mfma_f32_16x16x32_bf16 v[16:19], v[178:181], v[204:207], v[16:19]
	v_mfma_f32_16x16x32_bf16 v[4:7], v[170:173], v[220:223], v[4:7]
	v_mfma_f32_16x16x32_bf16 v[0:3], v[178:181], v[220:223], v[0:3]
	s_setprio 0
	s_barrier
	s_add_i32 s68, s68, 2
	s_add_u32 s54, s54, 0x100
	s_addc_u32 s55, s55, 0
	s_add_u32 s66, s66, 0x100
	s_addc_u32 s67, s67, 0
	s_cmp_gt_u32 s68, 13
	s_cbranch_scc0 .LBB0_1689
	s_and_b64 vcc, exec, s[30:31]
	s_cbranch_vccz .LBB0_1692
	s_barrier

.LBB0_1771:
	s_ashr_i32 s55, s54, 31
	s_lshl_b64 s[8:9], s[54:55], 21
	s_add_u32 s56, s74, s8
	s_addc_u32 s57, s75, s9
	s_and_b64 s[8:9], s[64:65], exec
	s_cselect_b32 s8, s57, s61
	s_cselect_b32 s9, s56, s60
	s_ashr_i32 s53, s52, 31
	s_lshl_b64 s[58:59], s[52:53], 21
	s_add_u32 s58, s22, s58
	s_addc_u32 s59, s23, s59
	s_and_b64 s[64:65], s[64:65], exec
	s_cselect_b32 s27, s59, s63
	s_cselect_b32 s31, s58, s62
	s_add_u32 s60, s60, 0x100080
	s_addc_u32 s61, s61, 0
	s_add_u32 s45, s62, 0x100
	v_mov_b32_e32 v0, 0
	s_addc_u32 s53, s63, 0
	s_mov_b32 s55, -2
	v_mov_b32_e32 v1, v0
	v_mov_b32_e32 v2, v0
	v_mov_b32_e32 v3, v0
	v_mov_b32_e32 v4, v0
	v_mov_b32_e32 v5, v0
	v_mov_b32_e32 v6, v0
	v_mov_b32_e32 v7, v0
	v_mov_b32_e32 v16, v0
	v_mov_b32_e32 v17, v0
	v_mov_b32_e32 v18, v0
	v_mov_b32_e32 v19, v0
	v_mov_b32_e32 v20, v0
	v_mov_b32_e32 v21, v0
	v_mov_b32_e32 v22, v0
	v_mov_b32_e32 v23, v0
	v_mov_b32_e32 v32, v0
	v_mov_b32_e32 v33, v0
	v_mov_b32_e32 v34, v0
	v_mov_b32_e32 v35, v0
	v_mov_b32_e32 v36, v0
	v_mov_b32_e32 v37, v0
	v_mov_b32_e32 v38, v0
	v_mov_b32_e32 v39, v0
	v_mov_b32_e32 v48, v0
	v_mov_b32_e32 v49, v0
	v_mov_b32_e32 v50, v0
	v_mov_b32_e32 v51, v0
	v_mov_b32_e32 v52, v0
	v_mov_b32_e32 v53, v0
	v_mov_b32_e32 v54, v0
	v_mov_b32_e32 v55, v0
	v_mov_b32_e32 v8, v0
	v_mov_b32_e32 v9, v0
	v_mov_b32_e32 v10, v0
	v_mov_b32_e32 v11, v0
	v_mov_b32_e32 v12, v0
	v_mov_b32_e32 v13, v0
	v_mov_b32_e32 v14, v0
	v_mov_b32_e32 v15, v0
	v_mov_b32_e32 v24, v0
	v_mov_b32_e32 v25, v0
	v_mov_b32_e32 v26, v0
	v_mov_b32_e32 v27, v0
	v_mov_b32_e32 v28, v0
	v_mov_b32_e32 v29, v0
	v_mov_b32_e32 v30, v0
	v_mov_b32_e32 v31, v0
	v_mov_b32_e32 v40, v0
	v_mov_b32_e32 v41, v0
	v_mov_b32_e32 v42, v0
	v_mov_b32_e32 v43, v0
	v_mov_b32_e32 v44, v0
	v_mov_b32_e32 v45, v0
	v_mov_b32_e32 v46, v0
	v_mov_b32_e32 v47, v0
	v_mov_b32_e32 v56, v0
	v_mov_b32_e32 v57, v0
	v_mov_b32_e32 v58, v0
	v_mov_b32_e32 v59, v0
	v_mov_b32_e32 v60, v0
	v_mov_b32_e32 v61, v0
	v_mov_b32_e32 v62, v0
	v_mov_b32_e32 v63, v0
	v_mov_b32_e32 v64, v0
	v_mov_b32_e32 v65, v0
	v_mov_b32_e32 v66, v0
	v_mov_b32_e32 v67, v0
	v_mov_b32_e32 v68, v0
	v_mov_b32_e32 v69, v0
	v_mov_b32_e32 v70, v0
	v_mov_b32_e32 v71, v0
	v_mov_b32_e32 v80, v0
	v_mov_b32_e32 v81, v0
	v_mov_b32_e32 v82, v0
	v_mov_b32_e32 v83, v0
	v_mov_b32_e32 v84, v0
	v_mov_b32_e32 v85, v0
	v_mov_b32_e32 v86, v0
	v_mov_b32_e32 v87, v0
	v_mov_b32_e32 v96, v0
	v_mov_b32_e32 v97, v0
	v_mov_b32_e32 v98, v0
	v_mov_b32_e32 v99, v0
	v_mov_b32_e32 v100, v0
	v_mov_b32_e32 v101, v0
	v_mov_b32_e32 v102, v0
	v_mov_b32_e32 v103, v0
	v_mov_b32_e32 v130, v0
	v_mov_b32_e32 v131, v0
	v_mov_b32_e32 v132, v0
	v_mov_b32_e32 v133, v0
	v_mov_b32_e32 v134, v0
	v_mov_b32_e32 v135, v0
	v_mov_b32_e32 v136, v0
	v_mov_b32_e32 v137, v0
	v_mov_b32_e32 v72, v0
	v_mov_b32_e32 v73, v0
	v_mov_b32_e32 v74, v0
	v_mov_b32_e32 v75, v0
	v_mov_b32_e32 v76, v0
	v_mov_b32_e32 v77, v0
	v_mov_b32_e32 v78, v0
	v_mov_b32_e32 v79, v0
	v_mov_b32_e32 v88, v0
	v_mov_b32_e32 v89, v0
	v_mov_b32_e32 v90, v0
	v_mov_b32_e32 v91, v0
	v_mov_b32_e32 v92, v0
	v_mov_b32_e32 v93, v0
	v_mov_b32_e32 v94, v0
	v_mov_b32_e32 v95, v0
	v_mov_b32_e32 v104, v0
	v_mov_b32_e32 v105, v0
	v_mov_b32_e32 v106, v0
	v_mov_b32_e32 v107, v0
	v_mov_b32_e32 v108, v0
	v_mov_b32_e32 v109, v0
	v_mov_b32_e32 v110, v0
	v_mov_b32_e32 v111, v0
	v_mov_b32_e32 v142, v0
	v_mov_b32_e32 v143, v0
	v_mov_b32_e32 v144, v0
	v_mov_b32_e32 v145, v0
	v_mov_b32_e32 v150, v0
	v_mov_b32_e32 v151, v0
	v_mov_b32_e32 v152, v0
	v_mov_b32_e32 v153, v0
	s_cmp_eq_u32 s70, 1
	s_cbranch_scc1 .LBB0_1772
	s_add_u32 s62, s60, 0xfff00080
	s_addc_u32 s63, s61, -1
	s_add_i32 s72, 0, 0x10000
	s_cmp_eq_u32 s55, 60
	s_cselect_b32 s65, s8, s63
	s_cselect_b32 s64, s9, s62
	s_cselect_b32 s63, s27, s53
	s_cselect_b32 s62, s31, s45
	s_add_i32 s76, 0, 0x14000
	v_add_u32_e32 v124, s72, v179
	v_add_u32_e32 v170, s76, v179
	ds_read_b128 v[112:115], v124
	ds_read_b128 v[116:119], v124 offset:1024
	ds_read_b128 v[120:123], v124 offset:2048
	ds_read_b128 v[124:127], v124 offset:3072
	ds_read_b128 v[138:141], v170
	ds_read_b128 v[146:149], v170 offset:1024
	ds_read_b128 v[166:169], v170 offset:2048
	ds_read_b128 v[170:173], v170 offset:3072
	v_lshl_add_u64 v[196:197], s[60:61], 0, v[162:163]
	s_add_i32 m0, s1, 0xc000
	ds_read_b128 v[174:177], v186
	ds_read_b128 v[188:191], v186 offset:1024
	ds_read_b128 v[192:195], v186 offset:2048
	ds_read_b128 v[200:203], v186 offset:3072
	ds_read_b128 v[204:207], v186 offset:4096
	ds_read_b128 v[216:219], v186 offset:5120
	ds_read_b128 v[220:223], v186 offset:6144
	ds_read_b128 v[224:227], v186 offset:7168
	global_load_lds_dwordx4 v[196:197], off
	v_lshl_add_u64 v[196:197], s[60:61], 0, v[164:165]
	s_add_i32 m0, s1, 0xe000
	s_nop 0
	global_load_lds_dwordx4 v[196:197], off
	s_waitcnt vmcnt(24)
	s_waitcnt lgkmcnt(0)
	s_barrier
	s_setprio 1
	s_waitcnt lgkmcnt(0)
	v_mfma_f32_16x16x32_bf16 v[150:153], v[112:115], v[174:177], v[150:153]
	v_mfma_f32_16x16x32_bf16 v[142:145], v[120:123], v[174:177], v[142:145]
	v_mfma_f32_16x16x32_bf16 v[108:111], v[112:115], v[192:195], v[108:111]
	v_mfma_f32_16x16x32_bf16 v[104:107], v[120:123], v[192:195], v[104:107]
	v_mfma_f32_16x16x32_bf16 v[92:95], v[112:115], v[204:207], v[92:95]
	v_mfma_f32_16x16x32_bf16 v[88:91], v[120:123], v[204:207], v[88:91]
	v_mfma_f32_16x16x32_bf16 v[76:79], v[112:115], v[220:223], v[76:79]
	v_mfma_f32_16x16x32_bf16 v[72:75], v[120:123], v[220:223], v[72:75]
	v_mfma_f32_16x16x32_bf16 v[150:153], v[116:119], v[188:191], v[150:153]
	v_mfma_f32_16x16x32_bf16 v[142:145], v[124:127], v[188:191], v[142:145]
	v_mfma_f32_16x16x32_bf16 v[108:111], v[116:119], v[200:203], v[108:111]
	v_mfma_f32_16x16x32_bf16 v[104:107], v[124:127], v[200:203], v[104:107]
	v_mfma_f32_16x16x32_bf16 v[92:95], v[116:119], v[216:219], v[92:95]
	v_mfma_f32_16x16x32_bf16 v[88:91], v[124:127], v[216:219], v[88:91]
	v_mfma_f32_16x16x32_bf16 v[76:79], v[116:119], v[224:227], v[76:79]
	v_mfma_f32_16x16x32_bf16 v[72:75], v[124:127], v[224:227], v[72:75]
	s_setprio 0
	s_setprio 1
	v_mfma_f32_16x16x32_bf16 v[134:137], v[138:141], v[174:177], v[134:137]
	v_mfma_f32_16x16x32_bf16 v[130:133], v[166:169], v[174:177], v[130:133]
	v_mfma_f32_16x16x32_bf16 v[100:103], v[138:141], v[192:195], v[100:103]
	v_mfma_f32_16x16x32_bf16 v[96:99], v[166:169], v[192:195], v[96:99]
	v_mfma_f32_16x16x32_bf16 v[84:87], v[138:141], v[204:207], v[84:87]
	v_mfma_f32_16x16x32_bf16 v[80:83], v[166:169], v[204:207], v[80:83]
	v_mfma_f32_16x16x32_bf16 v[68:71], v[138:141], v[220:223], v[68:71]
	v_mfma_f32_16x16x32_bf16 v[64:67], v[166:169], v[220:223], v[64:67]
	v_mfma_f32_16x16x32_bf16 v[134:137], v[146:149], v[188:191], v[134:137]
	v_mfma_f32_16x16x32_bf16 v[130:133], v[170:173], v[188:191], v[130:133]
	v_mfma_f32_16x16x32_bf16 v[100:103], v[146:149], v[200:203], v[100:103]
	v_mfma_f32_16x16x32_bf16 v[96:99], v[170:173], v[200:203], v[96:99]
	v_mfma_f32_16x16x32_bf16 v[84:87], v[146:149], v[216:219], v[84:87]
	v_mfma_f32_16x16x32_bf16 v[80:83], v[170:173], v[216:219], v[80:83]
	v_mfma_f32_16x16x32_bf16 v[68:71], v[146:149], v[224:227], v[68:71]
	v_mfma_f32_16x16x32_bf16 v[64:67], v[170:173], v[224:227], v[64:67]
	s_setprio 0
	s_barrier
	s_add_i32 s72, s72, s0
	v_lshl_add_u64 v[196:197], s[62:63], 0, v[128:129]
	s_mov_b32 m0, s72
	ds_read_b128 v[174:177], v186 offset:16384
	ds_read_b128 v[188:191], v186 offset:17408
	ds_read_b128 v[192:195], v186 offset:18432
	ds_read_b128 v[200:203], v186 offset:19456
	ds_read_b128 v[204:207], v186 offset:20480
	ds_read_b128 v[216:219], v186 offset:21504
	ds_read_b128 v[220:223], v186 offset:22528
	ds_read_b128 v[224:227], v186 offset:23552
	global_load_lds_dwordx4 v[196:197], off
	s_add_i32 m0, s72, 0x2000
	s_add_u32 s72, s62, 0x100000
	v_lshl_add_u64 v[208:209], s[62:63], 0, v[158:159]
	s_addc_u32 s73, s63, 0
	s_add_i32 s76, s76, s0
	global_load_lds_dwordx4 v[208:209], off
	v_lshl_add_u64 v[210:211], s[72:73], 0, v[128:129]
	s_mov_b32 m0, s76
	v_lshl_add_u64 v[214:215], s[64:65], 0, v[156:157]
	global_load_lds_dwordx4 v[210:211], off
	v_lshl_add_u64 v[210:211], s[72:73], 0, v[158:159]
	s_add_i32 m0, s76, 0x2000
	s_nop 0
	global_load_lds_dwordx4 v[210:211], off
	v_lshl_add_u64 v[210:211], s[64:65], 0, v[154:155]
	s_mov_b32 m0, s1
	s_nop 0
	global_load_lds_dwordx4 v[210:211], off
	s_mov_b32 m0, s33
	s_nop 0
	global_load_lds_dwordx4 v[214:215], off
	s_waitcnt vmcnt(24)
	s_waitcnt lgkmcnt(0)
	s_barrier
	s_setprio 1
	s_waitcnt lgkmcnt(0)
	v_mfma_f32_16x16x32_bf16 v[60:63], v[112:115], v[174:177], v[60:63]
	v_mfma_f32_16x16x32_bf16 v[56:59], v[120:123], v[174:177], v[56:59]
	v_mfma_f32_16x16x32_bf16 v[44:47], v[112:115], v[192:195], v[44:47]
	v_mfma_f32_16x16x32_bf16 v[40:43], v[120:123], v[192:195], v[40:43]
	v_mfma_f32_16x16x32_bf16 v[28:31], v[112:115], v[204:207], v[28:31]
	v_mfma_f32_16x16x32_bf16 v[24:27], v[120:123], v[204:207], v[24:27]
	v_mfma_f32_16x16x32_bf16 v[12:15], v[112:115], v[220:223], v[12:15]
	v_mfma_f32_16x16x32_bf16 v[8:11], v[120:123], v[220:223], v[8:11]
	v_mfma_f32_16x16x32_bf16 v[60:63], v[116:119], v[188:191], v[60:63]
	v_mfma_f32_16x16x32_bf16 v[56:59], v[124:127], v[188:191], v[56:59]
	v_mfma_f32_16x16x32_bf16 v[44:47], v[116:119], v[200:203], v[44:47]
	v_mfma_f32_16x16x32_bf16 v[40:43], v[124:127], v[200:203], v[40:43]
	v_mfma_f32_16x16x32_bf16 v[28:31], v[116:119], v[216:219], v[28:31]
	v_mfma_f32_16x16x32_bf16 v[24:27], v[124:127], v[216:219], v[24:27]
	v_mfma_f32_16x16x32_bf16 v[12:15], v[116:119], v[224:227], v[12:15]
	v_mfma_f32_16x16x32_bf16 v[8:11], v[124:127], v[224:227], v[8:11]
	s_setprio 0
	s_setprio 1
	v_mfma_f32_16x16x32_bf16 v[52:55], v[138:141], v[174:177], v[52:55]
	v_mfma_f32_16x16x32_bf16 v[48:51], v[166:169], v[174:177], v[48:51]
	v_mfma_f32_16x16x32_bf16 v[36:39], v[138:141], v[192:195], v[36:39]
	v_mfma_f32_16x16x32_bf16 v[32:35], v[166:169], v[192:195], v[32:35]
	v_mfma_f32_16x16x32_bf16 v[20:23], v[138:141], v[204:207], v[20:23]
	v_mfma_f32_16x16x32_bf16 v[16:19], v[166:169], v[204:207], v[16:19]
	v_mfma_f32_16x16x32_bf16 v[4:7], v[138:141], v[220:223], v[4:7]
	v_mfma_f32_16x16x32_bf16 v[0:3], v[166:169], v[220:223], v[0:3]
	v_mfma_f32_16x16x32_bf16 v[52:55], v[146:149], v[188:191], v[52:55]
	v_mfma_f32_16x16x32_bf16 v[48:51], v[170:173], v[188:191], v[48:51]
	v_mfma_f32_16x16x32_bf16 v[36:39], v[146:149], v[200:203], v[36:39]
	v_mfma_f32_16x16x32_bf16 v[32:35], v[170:173], v[200:203], v[32:35]
	v_mfma_f32_16x16x32_bf16 v[20:23], v[146:149], v[216:219], v[20:23]
	v_mfma_f32_16x16x32_bf16 v[16:19], v[170:173], v[216:219], v[16:19]
	v_mfma_f32_16x16x32_bf16 v[4:7], v[146:149], v[224:227], v[4:7]
	v_mfma_f32_16x16x32_bf16 v[0:3], v[170:173], v[224:227], v[0:3]
	s_setprio 0
	s_barrier
	s_branch .Lmlp2_mid

.Lmlp2_mid:
	s_add_i32 s72, 0, 0x18000
	s_add_i32 s73, 0, 0x1c000
	v_add_u32_e32 v124, s72, v179
	v_add_u32_e32 v170, s73, v179
	ds_read_b128 v[112:115], v124
	ds_read_b128 v[116:119], v124 offset:1024
	ds_read_b128 v[120:123], v124 offset:2048
	ds_read_b128 v[124:127], v124 offset:3072
	ds_read_b128 v[138:141], v170
	ds_read_b128 v[146:149], v170 offset:1024
	ds_read_b128 v[166:169], v170 offset:2048
	ds_read_b128 v[170:173], v170 offset:3072
	s_add_u32 s64, s64, 0x100000
	s_addc_u32 s65, s65, 0
	s_mov_b32 m0, s66
	v_lshl_add_u64 v[228:229], s[64:65], 0, v[154:155]
	ds_read_b128 v[174:177], v186 offset:32768
	ds_read_b128 v[188:191], v186 offset:33792
	ds_read_b128 v[192:195], v186 offset:34816
	ds_read_b128 v[200:203], v186 offset:35840
	ds_read_b128 v[204:207], v186 offset:36864
	ds_read_b128 v[216:219], v186 offset:37888
	ds_read_b128 v[220:223], v186 offset:38912
	ds_read_b128 v[224:227], v186 offset:39936
	global_load_lds_dwordx4 v[228:229], off
	v_lshl_add_u64 v[228:229], s[64:65], 0, v[156:157]
	s_mov_b32 m0, s67
	s_nop 0
	global_load_lds_dwordx4 v[228:229], off
	s_waitcnt vmcnt(8)
	s_waitcnt lgkmcnt(0)
	s_barrier
	s_setprio 1
	s_waitcnt lgkmcnt(0)
	v_mfma_f32_16x16x32_bf16 v[150:153], v[112:115], v[174:177], v[150:153]
	v_mfma_f32_16x16x32_bf16 v[142:145], v[120:123], v[174:177], v[142:145]
	v_mfma_f32_16x16x32_bf16 v[108:111], v[112:115], v[192:195], v[108:111]
	v_mfma_f32_16x16x32_bf16 v[104:107], v[120:123], v[192:195], v[104:107]
	v_mfma_f32_16x16x32_bf16 v[92:95], v[112:115], v[204:207], v[92:95]
	v_mfma_f32_16x16x32_bf16 v[88:91], v[120:123], v[204:207], v[88:91]
	v_mfma_f32_16x16x32_bf16 v[76:79], v[112:115], v[220:223], v[76:79]
	v_mfma_f32_16x16x32_bf16 v[72:75], v[120:123], v[220:223], v[72:75]
	v_mfma_f32_16x16x32_bf16 v[150:153], v[116:119], v[188:191], v[150:153]
	v_mfma_f32_16x16x32_bf16 v[142:145], v[124:127], v[188:191], v[142:145]
	v_mfma_f32_16x16x32_bf16 v[108:111], v[116:119], v[200:203], v[108:111]
	v_mfma_f32_16x16x32_bf16 v[104:107], v[124:127], v[200:203], v[104:107]
	v_mfma_f32_16x16x32_bf16 v[92:95], v[116:119], v[216:219], v[92:95]
	v_mfma_f32_16x16x32_bf16 v[88:91], v[124:127], v[216:219], v[88:91]
	v_mfma_f32_16x16x32_bf16 v[76:79], v[116:119], v[224:227], v[76:79]
	v_mfma_f32_16x16x32_bf16 v[72:75], v[124:127], v[224:227], v[72:75]
	s_setprio 0
	s_setprio 1
	v_mfma_f32_16x16x32_bf16 v[134:137], v[138:141], v[174:177], v[134:137]
	v_mfma_f32_16x16x32_bf16 v[130:133], v[166:169], v[174:177], v[130:133]
	v_mfma_f32_16x16x32_bf16 v[100:103], v[138:141], v[192:195], v[100:103]
	v_mfma_f32_16x16x32_bf16 v[96:99], v[166:169], v[192:195], v[96:99]
	v_mfma_f32_16x16x32_bf16 v[84:87], v[138:141], v[204:207], v[84:87]
	v_mfma_f32_16x16x32_bf16 v[80:83], v[166:169], v[204:207], v[80:83]
	v_mfma_f32_16x16x32_bf16 v[68:71], v[138:141], v[220:223], v[68:71]
	v_mfma_f32_16x16x32_bf16 v[64:67], v[166:169], v[220:223], v[64:67]
	v_mfma_f32_16x16x32_bf16 v[134:137], v[146:149], v[188:191], v[134:137]
	v_mfma_f32_16x16x32_bf16 v[130:133], v[170:173], v[188:191], v[130:133]
	v_mfma_f32_16x16x32_bf16 v[100:103], v[146:149], v[200:203], v[100:103]
	v_mfma_f32_16x16x32_bf16 v[96:99], v[170:173], v[200:203], v[96:99]
	v_mfma_f32_16x16x32_bf16 v[84:87], v[146:149], v[216:219], v[84:87]
	v_mfma_f32_16x16x32_bf16 v[80:83], v[170:173], v[216:219], v[80:83]
	v_mfma_f32_16x16x32_bf16 v[68:71], v[146:149], v[224:227], v[68:71]
	v_mfma_f32_16x16x32_bf16 v[64:67], v[170:173], v[224:227], v[64:67]
	s_setprio 0
	s_barrier
	s_add_i32 s64, s72, s0
	v_lshl_add_u64 v[196:197], v[196:197], 0, s[88:89]
	s_mov_b32 m0, s64
	ds_read_b128 v[174:177], v186 offset:49152
	ds_read_b128 v[188:191], v186 offset:50176
	ds_read_b128 v[192:195], v186 offset:51200
	ds_read_b128 v[200:203], v186 offset:52224
	ds_read_b128 v[204:207], v186 offset:53248
	ds_read_b128 v[216:219], v186 offset:54272
	ds_read_b128 v[220:223], v186 offset:55296
	ds_read_b128 v[224:227], v186 offset:56320
	global_load_lds_dwordx4 v[196:197], off
	s_add_i32 m0, s64, 0x2000
	s_add_u32 s62, s62, 0x100080
	v_lshl_add_u64 v[196:197], v[208:209], 0, s[88:89]
	s_addc_u32 s63, s63, 0
	s_add_i32 s64, s73, s0
	global_load_lds_dwordx4 v[196:197], off
	v_lshl_add_u64 v[196:197], s[62:63], 0, v[128:129]
	s_mov_b32 m0, s64
	s_nop 0
	global_load_lds_dwordx4 v[196:197], off
	v_lshl_add_u64 v[196:197], s[62:63], 0, v[158:159]
	s_add_i32 m0, s64, 0x2000
	s_nop 0
	global_load_lds_dwordx4 v[196:197], off
	v_lshl_add_u64 v[196:197], v[210:211], 0, s[88:89]
	s_mov_b32 m0, s68
	s_nop 0
	global_load_lds_dwordx4 v[196:197], off
	v_lshl_add_u64 v[196:197], v[214:215], 0, s[88:89]
	s_mov_b32 m0, s69
	s_nop 0
	global_load_lds_dwordx4 v[196:197], off
	s_waitcnt vmcnt(8)
	s_waitcnt lgkmcnt(0)
	s_barrier
	s_setprio 1
	s_waitcnt lgkmcnt(0)
	v_mfma_f32_16x16x32_bf16 v[60:63], v[112:115], v[174:177], v[60:63]
	v_mfma_f32_16x16x32_bf16 v[56:59], v[120:123], v[174:177], v[56:59]
	v_mfma_f32_16x16x32_bf16 v[44:47], v[112:115], v[192:195], v[44:47]
	v_mfma_f32_16x16x32_bf16 v[40:43], v[120:123], v[192:195], v[40:43]
	v_mfma_f32_16x16x32_bf16 v[28:31], v[112:115], v[204:207], v[28:31]
	v_mfma_f32_16x16x32_bf16 v[24:27], v[120:123], v[204:207], v[24:27]
	v_mfma_f32_16x16x32_bf16 v[12:15], v[112:115], v[220:223], v[12:15]
	v_mfma_f32_16x16x32_bf16 v[8:11], v[120:123], v[220:223], v[8:11]
	v_mfma_f32_16x16x32_bf16 v[60:63], v[116:119], v[188:191], v[60:63]
	v_mfma_f32_16x16x32_bf16 v[56:59], v[124:127], v[188:191], v[56:59]
	v_mfma_f32_16x16x32_bf16 v[44:47], v[116:119], v[200:203], v[44:47]
	v_mfma_f32_16x16x32_bf16 v[40:43], v[124:127], v[200:203], v[40:43]
	v_mfma_f32_16x16x32_bf16 v[28:31], v[116:119], v[216:219], v[28:31]
	v_mfma_f32_16x16x32_bf16 v[24:27], v[124:127], v[216:219], v[24:27]
	v_mfma_f32_16x16x32_bf16 v[12:15], v[116:119], v[224:227], v[12:15]
	v_mfma_f32_16x16x32_bf16 v[8:11], v[124:127], v[224:227], v[8:11]
	s_setprio 0
	s_setprio 1
	v_mfma_f32_16x16x32_bf16 v[52:55], v[138:141], v[174:177], v[52:55]
	v_mfma_f32_16x16x32_bf16 v[48:51], v[166:169], v[174:177], v[48:51]
	v_mfma_f32_16x16x32_bf16 v[36:39], v[138:141], v[192:195], v[36:39]
	v_mfma_f32_16x16x32_bf16 v[32:35], v[166:169], v[192:195], v[32:35]
	v_mfma_f32_16x16x32_bf16 v[20:23], v[138:141], v[204:207], v[20:23]
	v_mfma_f32_16x16x32_bf16 v[16:19], v[166:169], v[204:207], v[16:19]
	v_mfma_f32_16x16x32_bf16 v[4:7], v[138:141], v[220:223], v[4:7]
	v_mfma_f32_16x16x32_bf16 v[0:3], v[166:169], v[220:223], v[0:3]
	v_mfma_f32_16x16x32_bf16 v[52:55], v[146:149], v[188:191], v[52:55]
	v_mfma_f32_16x16x32_bf16 v[48:51], v[170:173], v[188:191], v[48:51]
	v_mfma_f32_16x16x32_bf16 v[36:39], v[146:149], v[200:203], v[36:39]
	v_mfma_f32_16x16x32_bf16 v[32:35], v[170:173], v[200:203], v[32:35]
	v_mfma_f32_16x16x32_bf16 v[20:23], v[146:149], v[216:219], v[20:23]
	v_mfma_f32_16x16x32_bf16 v[16:19], v[170:173], v[216:219], v[16:19]
	v_mfma_f32_16x16x32_bf16 v[4:7], v[146:149], v[224:227], v[4:7]
	v_mfma_f32_16x16x32_bf16 v[0:3], v[170:173], v[224:227], v[0:3]
	s_setprio 0
	s_barrier
	s_add_i32 s55, s55, 2
	s_add_u32 s60, s60, 0x100
	s_addc_u32 s61, s61, 0
	s_add_u32 s45, s45, 0x100
	s_addc_u32 s53, s53, 0
	s_cmp_gt_u32 s55, 61
	s_cbranch_scc0 .LBB0_1772
	s_and_b64 vcc, exec, s[50:51]
	s_cbranch_vccz .LBB0_1775
	s_barrier
